# nt weight stores + K-loop placement: gate/up +40B, both in-projections and out-projection moved next to a 64-byte line boundary
# speedup vs baseline: 1.0023x; 1.0023x over previous
; #define LAS __attribute__((address_space(3)))
; #define G8_STAGE(bufoff, gbase, voff) do { _Pragma("unroll") for (int _i = 0; _i < 2; ++_i) \
;         __builtin_amdgcn_global_load_lds((const unsigned*)((const char*)(gbase) + (voff)[_i]), (LAS unsigned*)(lds + (bufoff) + ldsw + _i * 8192), 16, 0, 0); } while (0)
; #define G8_LDA(dst, b, h) do { _Pragma("unroll") for (int m = 0; m < 4; ++m) _Pragma("unroll") for (int k = 0; k < 2; ++k) dst[m][k] = *(const LAS bf16x8*)(lds + G8_SA(b, h) + aoff + m * 2048 + k * 1024); } while (0)
; #define G8_LDB(dst, b, h) do { _Pragma("unroll") for (int n = 0; n < 2; ++n) _Pragma("unroll") for (int k = 0; k < 2; ++k) dst[n][k] = *(const LAS bf16x8*)(lds + G8_SB(b, h) + boff + n * 2048 + k * 1024); } while (0)
; #define G8_WAIT_L(n) asm volatile("s_waitcnt lgkmcnt(" #n ")" ::: "memory")
; #define G8_BAR __builtin_amdgcn_s_barrier()
; #define G8_SCHED __builtin_amdgcn_sched_barrier(0)
; template <class Epi, class Sched>
; __device__ __forceinline__ void gemm_phase(LAS unsigned char* lds, const int K, const Sched& S, const Epi& E) {
;     ...
;             G8_LDB(B0, 0, 0); G8_SCHED; G8_LDA(At, 0, 0); G8_STAGE(G8_SA(1, 1), a1, oc[1]);
;             if (last && has_next) S.aoff(nxt, tid, oc);
;             G8_WAIT_L(8); G8_BAR; G8_WAIT_L(0); G8_MMA(0, 0, At, B0); G8_BAR; G8_SCHED;
;             G8_LDB(B1, 0, 1); G8_STAGE(G8_SB(0, 0), b2, voffB);
;             G8_BAR; G8_WAIT_L(0); G8_MMA(0, 1, At, B1); G8_BAR;
;             G8_LDA(At, 0, 1); G8_STAGE(G8_SA(0, 0), a2, oc[0]);
;             G8_BAR; G8_WAIT_L(0); G8_MMA(1, 0, At, B0); G8_BAR; G8_SCHED;
;     __device__ __forceinline__ void init(f32x4 (&acc)[2][2][4][2], const g8::Unit& u, int wc, int fq) const {
;         const int colp = u.pn * 256 + wc * 32 + fq * 8;
; #pragma unroll
;         for (int b = 0; b < 2; ++b)
; #pragma unroll
;             for (int n = 0; n < 2; ++n) { const u32x2 bw = *(const LAS u32x2*)(biasL + colp + b * 128 + 4 * n);
;                 const f32x4 bv = (f32x4){__uint_as_float(bw[0] << 16), __uint_as_float(bw[0] & 0xffff0000u), __uint_as_float(bw[1] << 16), __uint_as_float(bw[1] & 0xffff0000u)};
; #pragma unroll
;                 for (int a = 0; a < 2; ++a)
; #pragma unroll
;                     for (int m = 0; m < 4; ++m) acc[a][b][m][n] = bv; } }
.LBB0_319:
	v_mov_b64_e32 v[18:19], 0x480
	v_cmp_lt_i64_e64 s[34:35], s[34:35], v[18:19]
	s_add_u32 s5, s36, 0x100
	v_mov_b64_e32 v[20:21], v[4:5]
	v_mov_b64_e32 v[24:25], v[8:9]
	v_mov_b64_e32 v[36:37], v[4:5]
	v_mov_b64_e32 v[40:41], v[8:9]
	v_mov_b64_e32 v[52:53], v[4:5]
	v_mov_b64_e32 v[56:57], v[8:9]
	v_mov_b64_e32 v[28:29], v[12:13]
	v_mov_b64_e32 v[32:33], v[16:17]
	v_mov_b64_e32 v[44:45], v[12:13]
	v_mov_b64_e32 v[48:49], v[16:17]
	v_mov_b64_e32 v[60:61], v[12:13]
	v_mov_b64_e32 v[64:65], v[16:17]
	v_mov_b64_e32 v[68:69], v[4:5]
	v_mov_b64_e32 v[72:73], v[8:9]
	v_mov_b64_e32 v[84:85], v[4:5]
	v_mov_b64_e32 v[88:89], v[8:9]
	v_mov_b64_e32 v[100:101], v[4:5]
	v_mov_b64_e32 v[104:105], v[8:9]
	v_mov_b64_e32 v[116:117], v[4:5]
	v_mov_b64_e32 v[120:121], v[8:9]
	v_mov_b64_e32 v[76:77], v[12:13]
	v_mov_b64_e32 v[80:81], v[16:17]
	v_mov_b64_e32 v[92:93], v[12:13]
	v_mov_b64_e32 v[96:97], v[16:17]
	v_mov_b64_e32 v[108:109], v[12:13]
	v_mov_b64_e32 v[112:113], v[16:17]
	v_mov_b64_e32 v[124:125], v[12:13]
	v_mov_b64_e32 v[128:129], v[16:17]
	s_addc_u32 s9, s37, 0
	s_mov_b32 s11, -2
	v_mov_b64_e32 v[18:19], v[2:3]
	v_mov_b64_e32 v[22:23], v[6:7]
	v_mov_b64_e32 v[34:35], v[2:3]
	v_mov_b64_e32 v[38:39], v[6:7]
	v_mov_b64_e32 v[50:51], v[2:3]
	v_mov_b64_e32 v[54:55], v[6:7]
	v_mov_b64_e32 v[26:27], v[10:11]
	v_mov_b64_e32 v[30:31], v[14:15]
	v_mov_b64_e32 v[42:43], v[10:11]
	v_mov_b64_e32 v[46:47], v[14:15]
	v_mov_b64_e32 v[58:59], v[10:11]
	v_mov_b64_e32 v[62:63], v[14:15]
	v_mov_b64_e32 v[66:67], v[2:3]
	v_mov_b64_e32 v[70:71], v[6:7]
	v_mov_b64_e32 v[82:83], v[2:3]
	v_mov_b64_e32 v[86:87], v[6:7]
	v_mov_b64_e32 v[98:99], v[2:3]
	v_mov_b64_e32 v[102:103], v[6:7]
	v_mov_b64_e32 v[114:115], v[2:3]
	v_mov_b64_e32 v[118:119], v[6:7]
	v_mov_b64_e32 v[74:75], v[10:11]
	v_mov_b64_e32 v[78:79], v[14:15]
	v_mov_b64_e32 v[90:91], v[10:11]
	v_mov_b64_e32 v[94:95], v[14:15]
	v_mov_b64_e32 v[106:107], v[10:11]
	v_mov_b64_e32 v[110:111], v[14:15]
	v_mov_b64_e32 v[122:123], v[10:11]
	v_mov_b64_e32 v[126:127], v[14:15]
	s_nop 0
	s_nop 0
	s_nop 0
	s_nop 0
	s_nop 0
.LBB0_320:
	s_add_u32 s36, s2, 0x100
	s_addc_u32 s37, s3, 0
	s_add_i32 s82, 0, 0x10000
	v_add_u32_e32 v0, s82, v145
	ds_read_b128 v[154:157], v0
	ds_read_b128 v[158:161], v0 offset:1024
	ds_read_b128 v[162:165], v0 offset:2048
	ds_read_b128 v[166:169], v0 offset:3072
	s_cmp_eq_u32 s11, 12
	s_cselect_b32 s49, s43, s37
	s_cselect_b32 s48, s42, s36
	s_cselect_b32 s47, s45, s9
	s_cselect_b32 s46, s44, s5
	v_lshl_add_u64 v[150:151], s[2:3], 0, v[148:149]
	s_add_i32 m0, s58, 0xc000
	ds_read_b128 v[170:173], v153
	ds_read_b128 v[174:177], v153 offset:1024
	ds_read_b128 v[178:181], v153 offset:2048
	ds_read_b128 v[182:185], v153 offset:3072
	ds_read_b128 v[186:189], v153 offset:4096
	ds_read_b128 v[190:193], v153 offset:5120
	ds_read_b128 v[194:197], v153 offset:6144
	ds_read_b128 v[198:201], v153 offset:7168
	global_load_lds_dwordx4 v[150:151], off
	v_lshl_add_u64 v[150:151], s[2:3], 0, v[146:147]
	s_add_i32 m0, s58, 0xe000
	s_nop 0
	global_load_lds_dwordx4 v[150:151], off
	s_waitcnt lgkmcnt(8)
	s_barrier
	s_waitcnt lgkmcnt(0)
	s_setprio 1
	s_waitcnt lgkmcnt(0)
	v_mfma_f32_16x16x32_bf16 v[126:129], v[154:157], v[170:173], v[126:129]
	v_mfma_f32_16x16x32_bf16 v[122:125], v[162:165], v[170:173], v[122:125]
	v_mfma_f32_16x16x32_bf16 v[110:113], v[154:157], v[178:181], v[110:113]
	v_mfma_f32_16x16x32_bf16 v[106:109], v[162:165], v[178:181], v[106:109]
	v_mfma_f32_16x16x32_bf16 v[94:97], v[154:157], v[186:189], v[94:97]
	v_mfma_f32_16x16x32_bf16 v[90:93], v[162:165], v[186:189], v[90:93]
	v_mfma_f32_16x16x32_bf16 v[78:81], v[154:157], v[194:197], v[78:81]
	v_mfma_f32_16x16x32_bf16 v[74:77], v[162:165], v[194:197], v[74:77]
	v_mfma_f32_16x16x32_bf16 v[126:129], v[158:161], v[174:177], v[126:129]
	v_mfma_f32_16x16x32_bf16 v[122:125], v[166:169], v[174:177], v[122:125]
	v_mfma_f32_16x16x32_bf16 v[110:113], v[158:161], v[182:185], v[110:113]
	v_mfma_f32_16x16x32_bf16 v[106:109], v[166:169], v[182:185], v[106:109]
	v_mfma_f32_16x16x32_bf16 v[94:97], v[158:161], v[190:193], v[94:97]
	v_mfma_f32_16x16x32_bf16 v[90:93], v[166:169], v[190:193], v[90:93]
	v_mfma_f32_16x16x32_bf16 v[78:81], v[158:161], v[198:201], v[78:81]
	v_mfma_f32_16x16x32_bf16 v[74:77], v[166:169], v[198:201], v[74:77]
	s_setprio 0
	s_barrier
	s_add_i32 s83, 0, 0x14000
	s_add_i32 s2, s82, s57
	v_add_u32_e32 v0, s83, v145
	v_lshl_add_u64 v[150:151], s[46:47], 0, v[132:133]
	s_mov_b32 m0, s2
	ds_read_b128 v[216:219], v0
	ds_read_b128 v[220:223], v0 offset:1024
	ds_read_b128 v[224:227], v0 offset:2048
	ds_read_b128 v[228:231], v0 offset:3072
	global_load_lds_dwordx4 v[150:151], off
	v_lshl_add_u64 v[232:233], s[46:47], 0, v[134:135]
	s_add_i32 m0, s2, 0x2000
	s_nop 0
	global_load_lds_dwordx4 v[232:233], off
	s_barrier
	s_waitcnt lgkmcnt(0)
	s_setprio 1
	s_waitcnt lgkmcnt(0)
	v_mfma_f32_16x16x32_bf16 v[118:121], v[216:219], v[170:173], v[118:121]
	v_mfma_f32_16x16x32_bf16 v[114:117], v[224:227], v[170:173], v[114:117]
	v_mfma_f32_16x16x32_bf16 v[102:105], v[216:219], v[178:181], v[102:105]
	v_mfma_f32_16x16x32_bf16 v[98:101], v[224:227], v[178:181], v[98:101]
	v_mfma_f32_16x16x32_bf16 v[86:89], v[216:219], v[186:189], v[86:89]
	v_mfma_f32_16x16x32_bf16 v[82:85], v[224:227], v[186:189], v[82:85]
	v_mfma_f32_16x16x32_bf16 v[70:73], v[216:219], v[194:197], v[70:73]
	v_mfma_f32_16x16x32_bf16 v[66:69], v[224:227], v[194:197], v[66:69]
	v_mfma_f32_16x16x32_bf16 v[118:121], v[220:223], v[174:177], v[118:121]
	v_mfma_f32_16x16x32_bf16 v[114:117], v[228:231], v[174:177], v[114:117]
	v_mfma_f32_16x16x32_bf16 v[102:105], v[220:223], v[182:185], v[102:105]
	v_mfma_f32_16x16x32_bf16 v[98:101], v[228:231], v[182:185], v[98:101]
	v_mfma_f32_16x16x32_bf16 v[86:89], v[220:223], v[190:193], v[86:89]
	v_mfma_f32_16x16x32_bf16 v[82:85], v[228:231], v[190:193], v[82:85]
	v_mfma_f32_16x16x32_bf16 v[70:73], v[220:223], v[198:201], v[70:73]
	v_mfma_f32_16x16x32_bf16 v[66:69], v[228:231], v[198:201], v[66:69]
	s_setprio 0
	s_mov_b32 m0, s58
	v_lshl_add_u64 v[234:235], s[48:49], 0, v[136:137]
	s_barrier
; #define G8_STAGE(bufoff, gbase, voff) do { _Pragma("unroll") for (int _i = 0; _i < 2; ++_i) \
;         __builtin_amdgcn_global_load_lds((const unsigned*)((const char*)(gbase) + (voff)[_i]), (LAS unsigned*)(lds + (bufoff) + ldsw + _i * 8192), 16, 0, 0); } while (0)
; #define G8_LDA(dst, b, h) do { _Pragma("unroll") for (int m = 0; m < 4; ++m) _Pragma("unroll") for (int k = 0; k < 2; ++k) dst[m][k] = *(const LAS bf16x8*)(lds + G8_SA(b, h) + aoff + m * 2048 + k * 1024); } while (0)
; #define G8_LDB(dst, b, h) do { _Pragma("unroll") for (int n = 0; n < 2; ++n) _Pragma("unroll") for (int k = 0; k < 2; ++k) dst[n][k] = *(const LAS bf16x8*)(lds + G8_SB(b, h) + boff + n * 2048 + k * 1024); } while (0)
; #define G8_MMA(ai, bj, At, Bt) do { __builtin_amdgcn_s_setprio(1); _Pragma("unroll") for (int m = 0; m < 4; ++m) _Pragma("unroll") for (int n = 0; n < 2; ++n) _Pragma("unroll") for (int k = 0; k < 2; ++k) \
;         acc[ai][bj][m][n] = __builtin_amdgcn_mfma_f32_16x16x32_bf16(Bt[n][k], At[m][k], acc[ai][bj][m][n], 0, 0, 0); __builtin_amdgcn_s_setprio(0); } while (0)
; #define G8_WAIT_V(n) asm volatile("s_waitcnt vmcnt(" #n ")" ::: "memory")
; #define G8_WAIT_L(n) asm volatile("s_waitcnt lgkmcnt(" #n ")" ::: "memory")
; #define G8_BAR __builtin_amdgcn_s_barrier()
; #define G8_SCHED __builtin_amdgcn_sched_barrier(0)
; template <class Epi, class Sched>
; __device__ __forceinline__ void gemm_phase(LAS unsigned char* lds, const int K, const Sched& S, const Epi& E) {
;     ...
;             G8_BAR; G8_WAIT_L(0); G8_MMA(0, 1, At, B1); G8_BAR;
;             G8_LDA(At, 0, 1); G8_STAGE(G8_SA(0, 0), a2, oc[0]);
;             G8_BAR; G8_WAIT_L(0); G8_MMA(1, 0, At, B0); G8_BAR; G8_SCHED;
;             G8_STAGE(G8_SB(0, 1), b2 + hstep, voffB);
;             G8_WAIT_V(6); G8_BAR; G8_MMA(1, 1, At, B1); G8_BAR;
;             G8_LDB(B0, 1, 0); G8_SCHED; G8_LDA(At, 1, 0); G8_STAGE(G8_SA(0, 1), a2, oc[1]);
;             G8_WAIT_L(8); G8_BAR; G8_WAIT_L(0); G8_MMA(0, 0, At, B0); G8_BAR; G8_SCHED;
;             G8_LDB(B1, 1, 1); G8_STAGE(G8_SB(1, 0), b3, voffB);
;             G8_BAR; G8_WAIT_L(0); G8_MMA(0, 1, At, B1); G8_BAR;
;             G8_LDA(At, 1, 1); G8_STAGE(G8_SA(1, 0), a3, oc[0]);
;             G8_BAR; G8_WAIT_L(0); G8_MMA(1, 0, At, B0); G8_BAR; G8_SCHED;
	ds_read_b128 v[170:173], v153 offset:16384
	ds_read_b128 v[174:177], v153 offset:17408
	ds_read_b128 v[178:181], v153 offset:18432
	ds_read_b128 v[182:185], v153 offset:19456
	ds_read_b128 v[186:189], v153 offset:20480
	ds_read_b128 v[190:193], v153 offset:21504
	ds_read_b128 v[194:197], v153 offset:22528
	ds_read_b128 v[198:201], v153 offset:23552
	global_load_lds_dwordx4 v[234:235], off
	v_lshl_add_u64 v[236:237], s[48:49], 0, v[140:141]
	s_mov_b32 m0, s59
	s_nop 0
	global_load_lds_dwordx4 v[236:237], off
	s_barrier
	s_waitcnt lgkmcnt(0)
	s_setprio 1
	s_waitcnt lgkmcnt(0)
	v_mfma_f32_16x16x32_bf16 v[62:65], v[154:157], v[170:173], v[62:65]
	v_mfma_f32_16x16x32_bf16 v[58:61], v[162:165], v[170:173], v[58:61]
	v_mfma_f32_16x16x32_bf16 v[46:49], v[154:157], v[178:181], v[46:49]
	v_mfma_f32_16x16x32_bf16 v[42:45], v[162:165], v[178:181], v[42:45]
	v_mfma_f32_16x16x32_bf16 v[30:33], v[154:157], v[186:189], v[30:33]
	v_mfma_f32_16x16x32_bf16 v[26:29], v[162:165], v[186:189], v[26:29]
	v_mfma_f32_16x16x32_bf16 v[14:17], v[154:157], v[194:197], v[14:17]
	v_mfma_f32_16x16x32_bf16 v[10:13], v[162:165], v[194:197], v[10:13]
	v_mfma_f32_16x16x32_bf16 v[62:65], v[158:161], v[174:177], v[62:65]
	v_mfma_f32_16x16x32_bf16 v[58:61], v[166:169], v[174:177], v[58:61]
	v_mfma_f32_16x16x32_bf16 v[46:49], v[158:161], v[182:185], v[46:49]
	v_mfma_f32_16x16x32_bf16 v[42:45], v[166:169], v[182:185], v[42:45]
	v_mfma_f32_16x16x32_bf16 v[30:33], v[158:161], v[190:193], v[30:33]
	v_mfma_f32_16x16x32_bf16 v[26:29], v[166:169], v[190:193], v[26:29]
	v_mfma_f32_16x16x32_bf16 v[14:17], v[158:161], v[198:201], v[14:17]
	v_mfma_f32_16x16x32_bf16 v[10:13], v[166:169], v[198:201], v[10:13]
	s_setprio 0
	s_barrier
	s_add_u32 s2, s46, 0x40000
	s_addc_u32 s3, s47, 0
	s_add_i32 s82, s83, s57
	v_lshl_add_u64 v[154:155], s[2:3], 0, v[132:133]
	s_mov_b32 m0, s82
	s_nop 0
	global_load_lds_dwordx4 v[154:155], off
	v_lshl_add_u64 v[154:155], s[2:3], 0, v[134:135]
	s_add_i32 m0, s82, 0x2000
	s_nop 0
	global_load_lds_dwordx4 v[154:155], off
	s_waitcnt vmcnt(6)
	s_barrier
	s_setprio 1
	v_mfma_f32_16x16x32_bf16 v[54:57], v[216:219], v[170:173], v[54:57]
	v_mfma_f32_16x16x32_bf16 v[50:53], v[224:227], v[170:173], v[50:53]
	v_mfma_f32_16x16x32_bf16 v[38:41], v[216:219], v[178:181], v[38:41]
	v_mfma_f32_16x16x32_bf16 v[34:37], v[224:227], v[178:181], v[34:37]
	v_mfma_f32_16x16x32_bf16 v[22:25], v[216:219], v[186:189], v[22:25]
	v_mfma_f32_16x16x32_bf16 v[18:21], v[224:227], v[186:189], v[18:21]
	v_mfma_f32_16x16x32_bf16 v[6:9], v[216:219], v[194:197], v[6:9]
	v_mfma_f32_16x16x32_bf16 v[2:5], v[224:227], v[194:197], v[2:5]
	v_mfma_f32_16x16x32_bf16 v[54:57], v[220:223], v[174:177], v[54:57]
	v_mfma_f32_16x16x32_bf16 v[50:53], v[228:231], v[174:177], v[50:53]
	v_mfma_f32_16x16x32_bf16 v[38:41], v[220:223], v[182:185], v[38:41]
	v_mfma_f32_16x16x32_bf16 v[34:37], v[228:231], v[182:185], v[34:37]
	v_mfma_f32_16x16x32_bf16 v[22:25], v[220:223], v[190:193], v[22:25]
	v_mfma_f32_16x16x32_bf16 v[18:21], v[228:231], v[190:193], v[18:21]
	v_mfma_f32_16x16x32_bf16 v[6:9], v[220:223], v[198:201], v[6:9]
	v_mfma_f32_16x16x32_bf16 v[2:5], v[228:231], v[198:201], v[2:5]
	s_setprio 0
	s_add_i32 s2, 0, 0x18000
	v_add_u32_e32 v0, s2, v145
	s_barrier
	ds_read_b128 v[154:157], v0
	ds_read_b128 v[158:161], v0 offset:1024
	ds_read_b128 v[162:165], v0 offset:2048
	ds_read_b128 v[166:169], v0 offset:3072
	s_mov_b32 m0, s60
	v_lshl_add_u64 v[216:217], s[48:49], 0, v[138:139]
	ds_read_b128 v[170:173], v153 offset:32768
	ds_read_b128 v[174:177], v153 offset:33792
	ds_read_b128 v[178:181], v153 offset:34816
	ds_read_b128 v[182:185], v153 offset:35840
	ds_read_b128 v[186:189], v153 offset:36864
	ds_read_b128 v[190:193], v153 offset:37888
	ds_read_b128 v[194:197], v153 offset:38912
	ds_read_b128 v[198:201], v153 offset:39936
	global_load_lds_dwordx4 v[216:217], off
	v_lshl_add_u64 v[216:217], s[48:49], 0, v[142:143]
	s_mov_b32 m0, s61
	s_nop 0
	global_load_lds_dwordx4 v[216:217], off
	s_waitcnt lgkmcnt(8)
	s_barrier
	s_waitcnt lgkmcnt(0)
	s_setprio 1
	s_waitcnt lgkmcnt(0)
	v_mfma_f32_16x16x32_bf16 v[126:129], v[154:157], v[170:173], v[126:129]
	v_mfma_f32_16x16x32_bf16 v[122:125], v[162:165], v[170:173], v[122:125]
	v_mfma_f32_16x16x32_bf16 v[110:113], v[154:157], v[178:181], v[110:113]
	v_mfma_f32_16x16x32_bf16 v[106:109], v[162:165], v[178:181], v[106:109]
	v_mfma_f32_16x16x32_bf16 v[94:97], v[154:157], v[186:189], v[94:97]
	v_mfma_f32_16x16x32_bf16 v[90:93], v[162:165], v[186:189], v[90:93]
	v_mfma_f32_16x16x32_bf16 v[78:81], v[154:157], v[194:197], v[78:81]
	v_mfma_f32_16x16x32_bf16 v[74:77], v[162:165], v[194:197], v[74:77]
	v_mfma_f32_16x16x32_bf16 v[126:129], v[158:161], v[174:177], v[126:129]
	v_mfma_f32_16x16x32_bf16 v[122:125], v[166:169], v[174:177], v[122:125]
	v_mfma_f32_16x16x32_bf16 v[110:113], v[158:161], v[182:185], v[110:113]
	v_mfma_f32_16x16x32_bf16 v[106:109], v[166:169], v[182:185], v[106:109]
	v_mfma_f32_16x16x32_bf16 v[94:97], v[158:161], v[190:193], v[94:97]
	v_mfma_f32_16x16x32_bf16 v[90:93], v[166:169], v[190:193], v[90:93]
	v_mfma_f32_16x16x32_bf16 v[78:81], v[158:161], v[198:201], v[78:81]
	v_mfma_f32_16x16x32_bf16 v[74:77], v[166:169], v[198:201], v[74:77]
	s_setprio 0
	s_barrier
	s_add_i32 s48, 0, 0x1c000
	s_add_i32 s2, s2, s57
	v_add_u32_e32 v0, s48, v145
	v_lshl_add_u64 v[150:151], v[150:151], 0, s[18:19]
	s_mov_b32 m0, s2
	ds_read_b128 v[216:219], v0
	ds_read_b128 v[220:223], v0 offset:1024
	ds_read_b128 v[224:227], v0 offset:2048
	ds_read_b128 v[228:231], v0 offset:3072
	global_load_lds_dwordx4 v[150:151], off
	v_lshl_add_u64 v[150:151], v[232:233], 0, s[18:19]
	s_add_i32 m0, s2, 0x2000
	s_nop 0
	global_load_lds_dwordx4 v[150:151], off
	s_barrier
; #define G8_STAGE(bufoff, gbase, voff) do { _Pragma("unroll") for (int _i = 0; _i < 2; ++_i) \
;         __builtin_amdgcn_global_load_lds((const unsigned*)((const char*)(gbase) + (voff)[_i]), (LAS unsigned*)(lds + (bufoff) + ldsw + _i * 8192), 16, 0, 0); } while (0)
; #define G8_MMA(ai, bj, At, Bt) do { __builtin_amdgcn_s_setprio(1); _Pragma("unroll") for (int m = 0; m < 4; ++m) _Pragma("unroll") for (int n = 0; n < 2; ++n) _Pragma("unroll") for (int k = 0; k < 2; ++k) \
;         acc[ai][bj][m][n] = __builtin_amdgcn_mfma_f32_16x16x32_bf16(Bt[n][k], At[m][k], acc[ai][bj][m][n], 0, 0, 0); __builtin_amdgcn_s_setprio(0); } while (0)
; #define G8_WAIT_V(n) asm volatile("s_waitcnt vmcnt(" #n ")" ::: "memory")
; #define G8_WAIT_L(n) asm volatile("s_waitcnt lgkmcnt(" #n ")" ::: "memory")
; #define G8_BAR __builtin_amdgcn_s_barrier()
; #define G8_SCHED __builtin_amdgcn_sched_barrier(0)
; template <class Epi, class Sched>
; __device__ __forceinline__ void gemm_phase(LAS unsigned char* lds, const int K, const Sched& S, const Epi& E) {
;     ...
;             G8_BAR; G8_WAIT_L(0); G8_MMA(1, 0, At, B0); G8_BAR; G8_SCHED;
;             G8_STAGE(G8_SB(1, 1), b3 + hstep, voffB);
;             G8_WAIT_V(6); G8_BAR; G8_MMA(1, 1, At, B1); G8_BAR;
;         }
;     __device__ __forceinline__ void operator()(const f32x4 (&acc)[2][2][4][2], const g8::Unit& u, int wr, int wc, int fr, int fq) const {
;         const int pn = u.pn; const int col0 = pn * 256 + wc * 32 + fq * 8;
;         bf16_t* gu = (bf16_t*)(ws + CD_GU); bf16_t* gvT = (bf16_t*)(ws + CD_GVT); bf16_t* gg = (bf16_t*)(ws + CD_GG); bf16_t* xr = (bf16_t*)(ws + CD_XR); float* stats = (float*)(ws + CD_STATS);
; #pragma unroll
;         for (int ai = 0; ai < 2; ++ai)
; #pragma unroll
;             for (int m = 0; m < 4; ++m) {
;                 const int t = u.pm * 256 + ai * 128 + wr * 64 + m * 16 + fr, sq = t & (SEQ - 1), b = t >> 13;
;                 f32x4 x[2][2];
; #pragma unroll
;                 for (int bj = 0; bj < 2; ++bj)
; #pragma unroll
;                     for (int n = 0; n < 2; ++n) { x[bj][n] = acc[ai][bj][m][n];
;                         if (pn < 13) {
;                             x[bj][n] = gelu4(x[bj][n]); } }
	s_waitcnt lgkmcnt(0)
	s_setprio 1
	s_waitcnt lgkmcnt(0)
	v_mfma_f32_16x16x32_bf16 v[118:121], v[216:219], v[170:173], v[118:121]
	v_mfma_f32_16x16x32_bf16 v[114:117], v[224:227], v[170:173], v[114:117]
	v_mfma_f32_16x16x32_bf16 v[102:105], v[216:219], v[178:181], v[102:105]
	v_mfma_f32_16x16x32_bf16 v[98:101], v[224:227], v[178:181], v[98:101]
	v_mfma_f32_16x16x32_bf16 v[86:89], v[216:219], v[186:189], v[86:89]
	v_mfma_f32_16x16x32_bf16 v[82:85], v[224:227], v[186:189], v[82:85]
	v_mfma_f32_16x16x32_bf16 v[70:73], v[216:219], v[194:197], v[70:73]
	v_mfma_f32_16x16x32_bf16 v[66:69], v[224:227], v[194:197], v[66:69]
	v_mfma_f32_16x16x32_bf16 v[118:121], v[220:223], v[174:177], v[118:121]
	v_mfma_f32_16x16x32_bf16 v[114:117], v[228:231], v[174:177], v[114:117]
	v_mfma_f32_16x16x32_bf16 v[102:105], v[220:223], v[182:185], v[102:105]
	v_mfma_f32_16x16x32_bf16 v[98:101], v[228:231], v[182:185], v[98:101]
	v_mfma_f32_16x16x32_bf16 v[86:89], v[220:223], v[190:193], v[86:89]
	v_mfma_f32_16x16x32_bf16 v[82:85], v[228:231], v[190:193], v[82:85]
	v_mfma_f32_16x16x32_bf16 v[70:73], v[220:223], v[198:201], v[70:73]
	v_mfma_f32_16x16x32_bf16 v[66:69], v[228:231], v[198:201], v[66:69]
	s_setprio 0
	s_mov_b32 m0, s64
	v_lshl_add_u64 v[150:151], v[234:235], 0, s[18:19]
	s_barrier
	ds_read_b128 v[170:173], v153 offset:49152
	ds_read_b128 v[174:177], v153 offset:50176
	ds_read_b128 v[178:181], v153 offset:51200
	ds_read_b128 v[182:185], v153 offset:52224
	ds_read_b128 v[186:189], v153 offset:53248
	ds_read_b128 v[190:193], v153 offset:54272
	ds_read_b128 v[194:197], v153 offset:55296
	ds_read_b128 v[198:201], v153 offset:56320
	global_load_lds_dwordx4 v[150:151], off
	v_lshl_add_u64 v[150:151], v[236:237], 0, s[18:19]
	s_mov_b32 m0, s65
	s_nop 0
	global_load_lds_dwordx4 v[150:151], off
	s_barrier
	s_waitcnt lgkmcnt(0)
	s_setprio 1
	s_waitcnt lgkmcnt(0)
	v_mfma_f32_16x16x32_bf16 v[62:65], v[154:157], v[170:173], v[62:65]
	v_mfma_f32_16x16x32_bf16 v[58:61], v[162:165], v[170:173], v[58:61]
	v_mfma_f32_16x16x32_bf16 v[46:49], v[154:157], v[178:181], v[46:49]
	v_mfma_f32_16x16x32_bf16 v[42:45], v[162:165], v[178:181], v[42:45]
	v_mfma_f32_16x16x32_bf16 v[30:33], v[154:157], v[186:189], v[30:33]
	v_mfma_f32_16x16x32_bf16 v[26:29], v[162:165], v[186:189], v[26:29]
	v_mfma_f32_16x16x32_bf16 v[14:17], v[154:157], v[194:197], v[14:17]
	v_mfma_f32_16x16x32_bf16 v[10:13], v[162:165], v[194:197], v[10:13]
	v_mfma_f32_16x16x32_bf16 v[62:65], v[158:161], v[174:177], v[62:65]
	v_mfma_f32_16x16x32_bf16 v[58:61], v[166:169], v[174:177], v[58:61]
	v_mfma_f32_16x16x32_bf16 v[46:49], v[158:161], v[182:185], v[46:49]
	v_mfma_f32_16x16x32_bf16 v[42:45], v[166:169], v[182:185], v[42:45]
	v_mfma_f32_16x16x32_bf16 v[30:33], v[158:161], v[190:193], v[30:33]
	v_mfma_f32_16x16x32_bf16 v[26:29], v[166:169], v[190:193], v[26:29]
	v_mfma_f32_16x16x32_bf16 v[14:17], v[158:161], v[198:201], v[14:17]
	v_mfma_f32_16x16x32_bf16 v[10:13], v[166:169], v[198:201], v[10:13]
	s_setprio 0
	s_barrier
	s_add_u32 s2, s46, 0x40080
	s_addc_u32 s3, s47, 0
	s_add_i32 s46, s48, s57
	v_lshl_add_u64 v[150:151], s[2:3], 0, v[132:133]
	s_mov_b32 m0, s46
	s_nop 0
	global_load_lds_dwordx4 v[150:151], off
	v_lshl_add_u64 v[150:151], s[2:3], 0, v[134:135]
	s_add_i32 m0, s46, 0x2000
	s_nop 0
	global_load_lds_dwordx4 v[150:151], off
	s_waitcnt vmcnt(6)
	s_barrier
	s_setprio 1
	v_mfma_f32_16x16x32_bf16 v[54:57], v[216:219], v[170:173], v[54:57]
	v_mfma_f32_16x16x32_bf16 v[50:53], v[224:227], v[170:173], v[50:53]
	v_mfma_f32_16x16x32_bf16 v[38:41], v[216:219], v[178:181], v[38:41]
	v_mfma_f32_16x16x32_bf16 v[34:37], v[224:227], v[178:181], v[34:37]
	v_mfma_f32_16x16x32_bf16 v[22:25], v[216:219], v[186:189], v[22:25]
	v_mfma_f32_16x16x32_bf16 v[18:21], v[224:227], v[186:189], v[18:21]
	v_mfma_f32_16x16x32_bf16 v[6:9], v[216:219], v[194:197], v[6:9]
	v_mfma_f32_16x16x32_bf16 v[2:5], v[224:227], v[194:197], v[2:5]
	v_mfma_f32_16x16x32_bf16 v[54:57], v[220:223], v[174:177], v[54:57]
	v_mfma_f32_16x16x32_bf16 v[50:53], v[228:231], v[174:177], v[50:53]
	v_mfma_f32_16x16x32_bf16 v[38:41], v[220:223], v[182:185], v[38:41]
	v_mfma_f32_16x16x32_bf16 v[34:37], v[228:231], v[182:185], v[34:37]
	v_mfma_f32_16x16x32_bf16 v[22:25], v[220:223], v[190:193], v[22:25]
	v_mfma_f32_16x16x32_bf16 v[18:21], v[228:231], v[190:193], v[18:21]
	v_mfma_f32_16x16x32_bf16 v[6:9], v[220:223], v[198:201], v[6:9]
	v_mfma_f32_16x16x32_bf16 v[2:5], v[228:231], v[198:201], v[2:5]
	s_setprio 0
	s_add_i32 s11, s11, 2
	s_add_u32 s5, s5, 0x100
	s_addc_u32 s9, s9, 0
	s_cmp_gt_u32 s11, 13
	s_mov_b64 s[2:3], s[36:37]
	s_barrier
	s_cbranch_scc0 .LBB0_320
	s_nop 0
	s_nop 0
	s_nop 0
	s_nop 0
	s_nop 0
	s_nop 0
	s_nop 0
	s_nop 0
	s_nop 0
	s_nop 0
	s_nop 0
	s_cmp_lt_i32 s14, 13
	s_cselect_b64 s[36:37], -1, 0
	s_and_b64 vcc, exec, s[36:37]
	s_cbranch_vccz .LBB0_325
	v_pk_mul_f32 v[154:155], v[126:127], v[126:127]
	v_pk_mul_f32 v[150:151], v[128:129], v[128:129]
	v_fmamk_f32 v0, v154, 0xbdd2d3e8, v202
	v_mul_f32_e32 v0, v126, v0
	v_exp_f32_e32 v154, v0
	v_fmamk_f32 v0, v155, 0xbdd2d3e8, v202
	v_mul_f32_e32 v0, v127, v0
	v_exp_f32_e32 v155, v0
	v_fmamk_f32 v0, v150, 0xbdd2d3e8, v202
	v_mul_f32_e32 v0, v128, v0
	v_exp_f32_e32 v150, v0
	v_fmamk_f32 v0, v151, 0xbdd2d3e8, v202
	v_mul_f32_e32 v0, v129, v0
	v_exp_f32_e32 v151, v0
	v_pk_add_f32 v[154:155], v[154:155], 1.0 op_sel_hi:[1,0]
	v_pk_add_f32 v[150:151], v[150:151], 1.0 op_sel_hi:[1,0]
	v_rcp_f32_e32 v154, v154
	v_rcp_f32_e32 v155, v155
	v_rcp_f32_e32 v150, v150
	v_rcp_f32_e32 v151, v151
	v_pk_mul_f32 v[126:127], v[126:127], v[154:155]
	v_pk_mul_f32 v[128:129], v[128:129], v[150:151]
	v_cndmask_b32_e64 v0, 0, 1, s[36:37]
	v_cmp_ne_u32_e64 s[2:3], 1, v0
	s_andn2_b64 vcc, exec, s[36:37]
	s_cbranch_vccz .LBB0_326

; #define LAS __attribute__((address_space(3)))
; #define G8_STAGE(bufoff, gbase, voff) do { _Pragma("unroll") for (int _i = 0; _i < 2; ++_i) \
;         __builtin_amdgcn_global_load_lds((const unsigned*)((const char*)(gbase) + (voff)[_i]), (LAS unsigned*)(lds + (bufoff) + ldsw + _i * 8192), 16, 0, 0); } while (0)
; #define G8_LDA(dst, b, h) do { _Pragma("unroll") for (int m = 0; m < 4; ++m) _Pragma("unroll") for (int k = 0; k < 2; ++k) dst[m][k] = *(const LAS bf16x8*)(lds + G8_SA(b, h) + aoff + m * 2048 + k * 1024); } while (0)
; #define G8_LDB(dst, b, h) do { _Pragma("unroll") for (int n = 0; n < 2; ++n) _Pragma("unroll") for (int k = 0; k < 2; ++k) dst[n][k] = *(const LAS bf16x8*)(lds + G8_SB(b, h) + boff + n * 2048 + k * 1024); } while (0)
; #define G8_WAIT_L(n) asm volatile("s_waitcnt lgkmcnt(" #n ")" ::: "memory")
; #define G8_BAR __builtin_amdgcn_s_barrier()
; #define G8_SCHED __builtin_amdgcn_sched_barrier(0)
; template <class Epi, class Sched>
; __device__ __forceinline__ void gemm_phase(LAS unsigned char* lds, const int K, const Sched& S, const Epi& E) {
;     ...
;             G8_LDB(B0, 0, 0); G8_SCHED; G8_LDA(At, 0, 0); G8_STAGE(G8_SA(1, 1), a1, oc[1]);
;             if (last && has_next) S.aoff(nxt, tid, oc);
;             G8_WAIT_L(8); G8_BAR; G8_WAIT_L(0); G8_MMA(0, 0, At, B0); G8_BAR; G8_SCHED;
;             G8_LDB(B1, 0, 1); G8_STAGE(G8_SB(0, 0), b2, voffB);
;             G8_BAR; G8_WAIT_L(0); G8_MMA(0, 1, At, B1); G8_BAR;
;             G8_LDA(At, 0, 1); G8_STAGE(G8_SA(0, 0), a2, oc[0]);
;             G8_BAR; G8_WAIT_L(0); G8_MMA(1, 0, At, B0); G8_BAR; G8_SCHED;
;     __device__ __forceinline__ void init(f32x4 (&acc)[2][2][4][2], const g8::Unit& u, int wc, int fq) const {
;         const int colp = u.pn * 256 + wc * 32 + fq * 8;
; #pragma unroll
;         for (int b = 0; b < 2; ++b)
; #pragma unroll
;             for (int n = 0; n < 2; ++n) { const u32x2 bw = *(const LAS u32x2*)(biasL + colp + b * 128 + 4 * n);
;                 const f32x4 bv = (f32x4){__uint_as_float(bw[0] << 16), __uint_as_float(bw[0] & 0xffff0000u), __uint_as_float(bw[1] << 16), __uint_as_float(bw[1] & 0xffff0000u)};
; #pragma unroll
;                 for (int a = 0; a < 2; ++a)
; #pragma unroll
;                     for (int m = 0; m < 4; ++m) acc[a][b][m][n] = bv; } }
.LBB0_486:
	v_mov_b64_e32 v[18:19], 0x440
	v_cmp_lt_i64_e64 s[34:35], s[34:35], v[18:19]
	s_add_u32 s3, s12, 0x100
	v_mov_b64_e32 v[20:21], v[8:9]
	v_mov_b64_e32 v[28:29], v[16:17]
	v_mov_b64_e32 v[36:37], v[8:9]
	v_mov_b64_e32 v[44:45], v[16:17]
	v_mov_b64_e32 v[52:53], v[8:9]
	v_mov_b64_e32 v[60:61], v[16:17]
	v_mov_b64_e32 v[24:25], v[4:5]
	v_mov_b64_e32 v[32:33], v[12:13]
	v_mov_b64_e32 v[40:41], v[4:5]
	v_mov_b64_e32 v[48:49], v[12:13]
	v_mov_b64_e32 v[56:57], v[4:5]
	v_mov_b64_e32 v[64:65], v[12:13]
	v_mov_b64_e32 v[68:69], v[8:9]
	v_mov_b64_e32 v[76:77], v[16:17]
	v_mov_b64_e32 v[84:85], v[8:9]
	v_mov_b64_e32 v[92:93], v[16:17]
	v_mov_b64_e32 v[100:101], v[8:9]
	v_mov_b64_e32 v[108:109], v[16:17]
	v_mov_b64_e32 v[116:117], v[8:9]
	v_mov_b64_e32 v[124:125], v[16:17]
	v_mov_b64_e32 v[72:73], v[4:5]
	v_mov_b64_e32 v[80:81], v[12:13]
	v_mov_b64_e32 v[88:89], v[4:5]
	v_mov_b64_e32 v[96:97], v[12:13]
	v_mov_b64_e32 v[104:105], v[4:5]
	v_mov_b64_e32 v[112:113], v[12:13]
	v_mov_b64_e32 v[120:121], v[4:5]
	v_mov_b64_e32 v[128:129], v[12:13]
	s_addc_u32 s14, s13, 0
	s_mov_b32 s47, -2
	v_mov_b64_e32 v[18:19], v[6:7]
	v_mov_b64_e32 v[26:27], v[14:15]
	v_mov_b64_e32 v[34:35], v[6:7]
	v_mov_b64_e32 v[42:43], v[14:15]
	v_mov_b64_e32 v[50:51], v[6:7]
	v_mov_b64_e32 v[58:59], v[14:15]
	v_mov_b64_e32 v[22:23], v[2:3]
	v_mov_b64_e32 v[30:31], v[10:11]
	v_mov_b64_e32 v[38:39], v[2:3]
	v_mov_b64_e32 v[46:47], v[10:11]
	v_mov_b64_e32 v[54:55], v[2:3]
	v_mov_b64_e32 v[62:63], v[10:11]
	v_mov_b64_e32 v[66:67], v[6:7]
	v_mov_b64_e32 v[74:75], v[14:15]
	v_mov_b64_e32 v[82:83], v[6:7]
	v_mov_b64_e32 v[90:91], v[14:15]
	v_mov_b64_e32 v[98:99], v[6:7]
	v_mov_b64_e32 v[106:107], v[14:15]
	v_mov_b64_e32 v[114:115], v[6:7]
	v_mov_b64_e32 v[122:123], v[14:15]
	v_mov_b64_e32 v[70:71], v[2:3]
	v_mov_b64_e32 v[78:79], v[10:11]
	v_mov_b64_e32 v[86:87], v[2:3]
	v_mov_b64_e32 v[94:95], v[10:11]
	v_mov_b64_e32 v[102:103], v[2:3]
	v_mov_b64_e32 v[110:111], v[10:11]
	v_mov_b64_e32 v[118:119], v[2:3]
	v_mov_b64_e32 v[126:127], v[10:11]
	s_nop 0
	s_nop 0
	s_nop 0
	s_nop 0
	s_nop 0
	s_nop 0
.LBB0_487:
	s_add_u32 s12, s0, 0x100
	s_addc_u32 s13, s1, 0
	s_add_i32 s49, 0, 0x10000
	v_add_u32_e32 v158, s49, v165
	ds_read_b128 v[130:133], v158
	ds_read_b128 v[134:137], v158 offset:1024
	ds_read_b128 v[154:157], v158 offset:2048
	ds_read_b128 v[158:161], v158 offset:3072
	s_cmp_eq_u32 s47, 12
	s_cselect_b32 s43, s23, s13
	s_cselect_b32 s42, s22, s12
	s_cselect_b32 s39, s37, s14
	s_cselect_b32 s38, s36, s3
	v_lshl_add_u64 v[162:163], s[0:1], 0, v[152:153]
	s_add_i32 m0, s76, 0xc000
	ds_read_b128 v[168:171], v167
	ds_read_b128 v[172:175], v167 offset:1024
	ds_read_b128 v[176:179], v167 offset:2048
	ds_read_b128 v[180:183], v167 offset:3072
	ds_read_b128 v[184:187], v167 offset:4096
	ds_read_b128 v[188:191], v167 offset:5120
	ds_read_b128 v[192:195], v167 offset:6144
	ds_read_b128 v[196:199], v167 offset:7168
	global_load_lds_dwordx4 v[162:163], off
	v_lshl_add_u64 v[162:163], s[0:1], 0, v[150:151]
	s_add_i32 m0, s76, 0xe000
	s_nop 0
	global_load_lds_dwordx4 v[162:163], off
	s_waitcnt lgkmcnt(8)
	s_barrier
	s_waitcnt lgkmcnt(0)
	s_setprio 1
	s_waitcnt lgkmcnt(0)
	v_mfma_f32_16x16x32_bf16 v[126:129], v[130:133], v[168:171], v[126:129]
	v_mfma_f32_16x16x32_bf16 v[118:121], v[154:157], v[168:171], v[118:121]
	v_mfma_f32_16x16x32_bf16 v[110:113], v[130:133], v[176:179], v[110:113]
	v_mfma_f32_16x16x32_bf16 v[102:105], v[154:157], v[176:179], v[102:105]
	v_mfma_f32_16x16x32_bf16 v[94:97], v[130:133], v[184:187], v[94:97]
	v_mfma_f32_16x16x32_bf16 v[86:89], v[154:157], v[184:187], v[86:89]
	v_mfma_f32_16x16x32_bf16 v[78:81], v[130:133], v[192:195], v[78:81]
	v_mfma_f32_16x16x32_bf16 v[70:73], v[154:157], v[192:195], v[70:73]
	v_mfma_f32_16x16x32_bf16 v[126:129], v[134:137], v[172:175], v[126:129]
	v_mfma_f32_16x16x32_bf16 v[118:121], v[158:161], v[172:175], v[118:121]
	v_mfma_f32_16x16x32_bf16 v[110:113], v[134:137], v[180:183], v[110:113]
	v_mfma_f32_16x16x32_bf16 v[102:105], v[158:161], v[180:183], v[102:105]
	v_mfma_f32_16x16x32_bf16 v[94:97], v[134:137], v[188:191], v[94:97]
	v_mfma_f32_16x16x32_bf16 v[86:89], v[158:161], v[188:191], v[86:89]
	v_mfma_f32_16x16x32_bf16 v[78:81], v[134:137], v[196:199], v[78:81]
	v_mfma_f32_16x16x32_bf16 v[70:73], v[158:161], v[196:199], v[70:73]
	s_setprio 0
	s_barrier
	s_add_i32 s54, 0, 0x14000
	v_add_u32_e32 v162, s54, v165
	s_add_i32 s0, s49, s65
	ds_read_b128 v[216:219], v162
	ds_read_b128 v[220:223], v162 offset:1024
	ds_read_b128 v[224:227], v162 offset:2048
	ds_read_b128 v[228:231], v162 offset:3072
	v_lshl_add_u64 v[162:163], s[38:39], 0, v[0:1]
	s_mov_b32 m0, s0
	v_lshl_add_u64 v[200:201], s[38:39], 0, v[140:141]
	global_load_lds_dwordx4 v[162:163], off
	s_add_i32 m0, s0, 0x2000
	s_nop 0
	global_load_lds_dwordx4 v[200:201], off
	s_barrier
	s_waitcnt lgkmcnt(0)
	s_setprio 1
	s_waitcnt lgkmcnt(0)
	v_mfma_f32_16x16x32_bf16 v[122:125], v[216:219], v[168:171], v[122:125]
	v_mfma_f32_16x16x32_bf16 v[114:117], v[224:227], v[168:171], v[114:117]
	v_mfma_f32_16x16x32_bf16 v[106:109], v[216:219], v[176:179], v[106:109]
	v_mfma_f32_16x16x32_bf16 v[98:101], v[224:227], v[176:179], v[98:101]
	v_mfma_f32_16x16x32_bf16 v[90:93], v[216:219], v[184:187], v[90:93]
	v_mfma_f32_16x16x32_bf16 v[82:85], v[224:227], v[184:187], v[82:85]
	v_mfma_f32_16x16x32_bf16 v[74:77], v[216:219], v[192:195], v[74:77]
	v_mfma_f32_16x16x32_bf16 v[66:69], v[224:227], v[192:195], v[66:69]
	v_mfma_f32_16x16x32_bf16 v[122:125], v[220:223], v[172:175], v[122:125]
	v_mfma_f32_16x16x32_bf16 v[114:117], v[228:231], v[172:175], v[114:117]
	v_mfma_f32_16x16x32_bf16 v[106:109], v[220:223], v[180:183], v[106:109]
	v_mfma_f32_16x16x32_bf16 v[98:101], v[228:231], v[180:183], v[98:101]
	v_mfma_f32_16x16x32_bf16 v[90:93], v[220:223], v[188:191], v[90:93]
	v_mfma_f32_16x16x32_bf16 v[82:85], v[228:231], v[188:191], v[82:85]
	v_mfma_f32_16x16x32_bf16 v[74:77], v[220:223], v[196:199], v[74:77]
	v_mfma_f32_16x16x32_bf16 v[66:69], v[228:231], v[196:199], v[66:69]
	s_setprio 0
	s_mov_b32 m0, s76
	v_lshl_add_u64 v[232:233], s[42:43], 0, v[142:143]
	s_barrier
; #define G8_STAGE(bufoff, gbase, voff) do { _Pragma("unroll") for (int _i = 0; _i < 2; ++_i) \
;         __builtin_amdgcn_global_load_lds((const unsigned*)((const char*)(gbase) + (voff)[_i]), (LAS unsigned*)(lds + (bufoff) + ldsw + _i * 8192), 16, 0, 0); } while (0)
; #define G8_LDA(dst, b, h) do { _Pragma("unroll") for (int m = 0; m < 4; ++m) _Pragma("unroll") for (int k = 0; k < 2; ++k) dst[m][k] = *(const LAS bf16x8*)(lds + G8_SA(b, h) + aoff + m * 2048 + k * 1024); } while (0)
; #define G8_LDB(dst, b, h) do { _Pragma("unroll") for (int n = 0; n < 2; ++n) _Pragma("unroll") for (int k = 0; k < 2; ++k) dst[n][k] = *(const LAS bf16x8*)(lds + G8_SB(b, h) + boff + n * 2048 + k * 1024); } while (0)
; #define G8_MMA(ai, bj, At, Bt) do { __builtin_amdgcn_s_setprio(1); _Pragma("unroll") for (int m = 0; m < 4; ++m) _Pragma("unroll") for (int n = 0; n < 2; ++n) _Pragma("unroll") for (int k = 0; k < 2; ++k) \
;         acc[ai][bj][m][n] = __builtin_amdgcn_mfma_f32_16x16x32_bf16(Bt[n][k], At[m][k], acc[ai][bj][m][n], 0, 0, 0); __builtin_amdgcn_s_setprio(0); } while (0)
; #define G8_WAIT_V(n) asm volatile("s_waitcnt vmcnt(" #n ")" ::: "memory")
; #define G8_WAIT_L(n) asm volatile("s_waitcnt lgkmcnt(" #n ")" ::: "memory")
; #define G8_BAR __builtin_amdgcn_s_barrier()
; #define G8_SCHED __builtin_amdgcn_sched_barrier(0)
; template <class Epi, class Sched>
; __device__ __forceinline__ void gemm_phase(LAS unsigned char* lds, const int K, const Sched& S, const Epi& E) {
;     ...
;             G8_BAR; G8_WAIT_L(0); G8_MMA(0, 1, At, B1); G8_BAR;
;             G8_LDA(At, 0, 1); G8_STAGE(G8_SA(0, 0), a2, oc[0]);
;             G8_BAR; G8_WAIT_L(0); G8_MMA(1, 0, At, B0); G8_BAR; G8_SCHED;
;             G8_STAGE(G8_SB(0, 1), b2 + hstep, voffB);
;             G8_WAIT_V(6); G8_BAR; G8_MMA(1, 1, At, B1); G8_BAR;
;             G8_LDB(B0, 1, 0); G8_SCHED; G8_LDA(At, 1, 0); G8_STAGE(G8_SA(0, 1), a2, oc[1]);
;             G8_WAIT_L(8); G8_BAR; G8_WAIT_L(0); G8_MMA(0, 0, At, B0); G8_BAR; G8_SCHED;
;             G8_LDB(B1, 1, 1); G8_STAGE(G8_SB(1, 0), b3, voffB);
;             G8_BAR; G8_WAIT_L(0); G8_MMA(0, 1, At, B1); G8_BAR;
;             G8_LDA(At, 1, 1); G8_STAGE(G8_SA(1, 0), a3, oc[0]);
;             G8_BAR; G8_WAIT_L(0); G8_MMA(1, 0, At, B0); G8_BAR; G8_SCHED;
	ds_read_b128 v[168:171], v167 offset:16384
	ds_read_b128 v[172:175], v167 offset:17408
	ds_read_b128 v[176:179], v167 offset:18432
	ds_read_b128 v[180:183], v167 offset:19456
	ds_read_b128 v[184:187], v167 offset:20480
	ds_read_b128 v[188:191], v167 offset:21504
	ds_read_b128 v[192:195], v167 offset:22528
	ds_read_b128 v[196:199], v167 offset:23552
	global_load_lds_dwordx4 v[232:233], off
	v_lshl_add_u64 v[234:235], s[42:43], 0, v[146:147]
	s_mov_b32 m0, s77
	s_nop 0
	global_load_lds_dwordx4 v[234:235], off
	s_barrier
	s_waitcnt lgkmcnt(0)
	s_setprio 1
	s_waitcnt lgkmcnt(0)
	v_mfma_f32_16x16x32_bf16 v[62:65], v[130:133], v[168:171], v[62:65]
	v_mfma_f32_16x16x32_bf16 v[54:57], v[154:157], v[168:171], v[54:57]
	v_mfma_f32_16x16x32_bf16 v[46:49], v[130:133], v[176:179], v[46:49]
	v_mfma_f32_16x16x32_bf16 v[38:41], v[154:157], v[176:179], v[38:41]
	v_mfma_f32_16x16x32_bf16 v[30:33], v[130:133], v[184:187], v[30:33]
	v_mfma_f32_16x16x32_bf16 v[22:25], v[154:157], v[184:187], v[22:25]
	v_mfma_f32_16x16x32_bf16 v[10:13], v[130:133], v[192:195], v[10:13]
	v_mfma_f32_16x16x32_bf16 v[2:5], v[154:157], v[192:195], v[2:5]
	v_mfma_f32_16x16x32_bf16 v[62:65], v[134:137], v[172:175], v[62:65]
	v_mfma_f32_16x16x32_bf16 v[54:57], v[158:161], v[172:175], v[54:57]
	v_mfma_f32_16x16x32_bf16 v[46:49], v[134:137], v[180:183], v[46:49]
	v_mfma_f32_16x16x32_bf16 v[38:41], v[158:161], v[180:183], v[38:41]
	v_mfma_f32_16x16x32_bf16 v[30:33], v[134:137], v[188:191], v[30:33]
	v_mfma_f32_16x16x32_bf16 v[22:25], v[158:161], v[188:191], v[22:25]
	v_mfma_f32_16x16x32_bf16 v[10:13], v[134:137], v[196:199], v[10:13]
	v_mfma_f32_16x16x32_bf16 v[2:5], v[158:161], v[196:199], v[2:5]
	s_setprio 0
	s_barrier
	s_add_u32 s0, s38, 0x40000
	s_addc_u32 s1, s39, 0
	s_add_i32 s49, s54, s65
	v_lshl_add_u64 v[130:131], s[0:1], 0, v[0:1]
	s_mov_b32 m0, s49
	s_nop 0
	global_load_lds_dwordx4 v[130:131], off
	v_lshl_add_u64 v[130:131], s[0:1], 0, v[140:141]
	s_add_i32 m0, s49, 0x2000
	s_nop 0
	global_load_lds_dwordx4 v[130:131], off
	s_waitcnt vmcnt(6)
	s_barrier
	s_setprio 1
	v_mfma_f32_16x16x32_bf16 v[58:61], v[216:219], v[168:171], v[58:61]
	v_mfma_f32_16x16x32_bf16 v[50:53], v[224:227], v[168:171], v[50:53]
	v_mfma_f32_16x16x32_bf16 v[42:45], v[216:219], v[176:179], v[42:45]
	v_mfma_f32_16x16x32_bf16 v[34:37], v[224:227], v[176:179], v[34:37]
	v_mfma_f32_16x16x32_bf16 v[26:29], v[216:219], v[184:187], v[26:29]
	v_mfma_f32_16x16x32_bf16 v[18:21], v[224:227], v[184:187], v[18:21]
	v_mfma_f32_16x16x32_bf16 v[14:17], v[216:219], v[192:195], v[14:17]
	v_mfma_f32_16x16x32_bf16 v[6:9], v[224:227], v[192:195], v[6:9]
	v_mfma_f32_16x16x32_bf16 v[58:61], v[220:223], v[172:175], v[58:61]
	v_mfma_f32_16x16x32_bf16 v[50:53], v[228:231], v[172:175], v[50:53]
	v_mfma_f32_16x16x32_bf16 v[42:45], v[220:223], v[180:183], v[42:45]
	v_mfma_f32_16x16x32_bf16 v[34:37], v[228:231], v[180:183], v[34:37]
	v_mfma_f32_16x16x32_bf16 v[26:29], v[220:223], v[188:191], v[26:29]
	v_mfma_f32_16x16x32_bf16 v[18:21], v[228:231], v[188:191], v[18:21]
	v_mfma_f32_16x16x32_bf16 v[14:17], v[220:223], v[196:199], v[14:17]
	v_mfma_f32_16x16x32_bf16 v[6:9], v[228:231], v[196:199], v[6:9]
	s_setprio 0
	s_add_i32 s0, 0, 0x18000
	v_add_u32_e32 v158, s0, v165
	s_barrier
	ds_read_b128 v[130:133], v158
	ds_read_b128 v[134:137], v158 offset:1024
	ds_read_b128 v[154:157], v158 offset:2048
	ds_read_b128 v[158:161], v158 offset:3072
	s_mov_b32 m0, s78
	v_lshl_add_u64 v[216:217], s[42:43], 0, v[144:145]
	ds_read_b128 v[168:171], v167 offset:32768
	ds_read_b128 v[172:175], v167 offset:33792
	ds_read_b128 v[176:179], v167 offset:34816
	ds_read_b128 v[180:183], v167 offset:35840
	ds_read_b128 v[184:187], v167 offset:36864
	ds_read_b128 v[188:191], v167 offset:37888
	ds_read_b128 v[192:195], v167 offset:38912
	ds_read_b128 v[196:199], v167 offset:39936
	global_load_lds_dwordx4 v[216:217], off
	v_lshl_add_u64 v[216:217], s[42:43], 0, v[148:149]
	s_mov_b32 m0, s79
	s_nop 0
	global_load_lds_dwordx4 v[216:217], off
	s_waitcnt lgkmcnt(8)
	s_barrier
	s_waitcnt lgkmcnt(0)
	s_setprio 1
	s_waitcnt lgkmcnt(0)
	v_mfma_f32_16x16x32_bf16 v[126:129], v[130:133], v[168:171], v[126:129]
	v_mfma_f32_16x16x32_bf16 v[118:121], v[154:157], v[168:171], v[118:121]
	v_mfma_f32_16x16x32_bf16 v[110:113], v[130:133], v[176:179], v[110:113]
	v_mfma_f32_16x16x32_bf16 v[102:105], v[154:157], v[176:179], v[102:105]
	v_mfma_f32_16x16x32_bf16 v[94:97], v[130:133], v[184:187], v[94:97]
	v_mfma_f32_16x16x32_bf16 v[86:89], v[154:157], v[184:187], v[86:89]
	v_mfma_f32_16x16x32_bf16 v[78:81], v[130:133], v[192:195], v[78:81]
	v_mfma_f32_16x16x32_bf16 v[70:73], v[154:157], v[192:195], v[70:73]
	v_mfma_f32_16x16x32_bf16 v[126:129], v[134:137], v[172:175], v[126:129]
	v_mfma_f32_16x16x32_bf16 v[118:121], v[158:161], v[172:175], v[118:121]
	v_mfma_f32_16x16x32_bf16 v[110:113], v[134:137], v[180:183], v[110:113]
	v_mfma_f32_16x16x32_bf16 v[102:105], v[158:161], v[180:183], v[102:105]
	v_mfma_f32_16x16x32_bf16 v[94:97], v[134:137], v[188:191], v[94:97]
	v_mfma_f32_16x16x32_bf16 v[86:89], v[158:161], v[188:191], v[86:89]
	v_mfma_f32_16x16x32_bf16 v[78:81], v[134:137], v[196:199], v[78:81]
	v_mfma_f32_16x16x32_bf16 v[70:73], v[158:161], v[196:199], v[70:73]
	s_setprio 0
	s_barrier
	s_add_i32 s42, 0, 0x1c000
	s_add_i32 s0, s0, s65
	v_add_u32_e32 v213, s42, v165
	v_lshl_add_u64 v[162:163], v[162:163], 0, s[18:19]
	s_mov_b32 m0, s0
	ds_read_b128 v[216:219], v213
	ds_read_b128 v[220:223], v213 offset:1024
	ds_read_b128 v[224:227], v213 offset:2048
	ds_read_b128 v[228:231], v213 offset:3072
	global_load_lds_dwordx4 v[162:163], off
	v_lshl_add_u64 v[162:163], v[200:201], 0, s[18:19]
	s_add_i32 m0, s0, 0x2000
	s_nop 0
	global_load_lds_dwordx4 v[162:163], off
	s_barrier
; #define G8_STAGE(bufoff, gbase, voff) do { _Pragma("unroll") for (int _i = 0; _i < 2; ++_i) \
;         __builtin_amdgcn_global_load_lds((const unsigned*)((const char*)(gbase) + (voff)[_i]), (LAS unsigned*)(lds + (bufoff) + ldsw + _i * 8192), 16, 0, 0); } while (0)
; #define G8_LDA(dst, b, h) do { _Pragma("unroll") for (int m = 0; m < 4; ++m) _Pragma("unroll") for (int k = 0; k < 2; ++k) dst[m][k] = *(const LAS bf16x8*)(lds + G8_SA(b, h) + aoff + m * 2048 + k * 1024); } while (0)
; #define G8_MMA(ai, bj, At, Bt) do { __builtin_amdgcn_s_setprio(1); _Pragma("unroll") for (int m = 0; m < 4; ++m) _Pragma("unroll") for (int n = 0; n < 2; ++n) _Pragma("unroll") for (int k = 0; k < 2; ++k) \
;         acc[ai][bj][m][n] = __builtin_amdgcn_mfma_f32_16x16x32_bf16(Bt[n][k], At[m][k], acc[ai][bj][m][n], 0, 0, 0); __builtin_amdgcn_s_setprio(0); } while (0)
; #define G8_WAIT_V(n) asm volatile("s_waitcnt vmcnt(" #n ")" ::: "memory")
; #define G8_WAIT_L(n) asm volatile("s_waitcnt lgkmcnt(" #n ")" ::: "memory")
; #define G8_BAR __builtin_amdgcn_s_barrier()
; #define G8_SCHED __builtin_amdgcn_sched_barrier(0)
; template <class Epi, class Sched>
; __device__ __forceinline__ void gemm_phase(LAS unsigned char* lds, const int K, const Sched& S, const Epi& E) {
;     ...
;             G8_BAR; G8_WAIT_L(0); G8_MMA(0, 1, At, B1); G8_BAR;
;             G8_LDA(At, 1, 1); G8_STAGE(G8_SA(1, 0), a3, oc[0]);
;             G8_BAR; G8_WAIT_L(0); G8_MMA(1, 0, At, B0); G8_BAR; G8_SCHED;
;             G8_STAGE(G8_SB(1, 1), b3 + hstep, voffB);
;             G8_WAIT_V(6); G8_BAR; G8_MMA(1, 1, At, B1); G8_BAR;
;         }
	s_waitcnt lgkmcnt(0)
	s_setprio 1
	s_waitcnt lgkmcnt(0)
	v_mfma_f32_16x16x32_bf16 v[122:125], v[216:219], v[168:171], v[122:125]
	v_mfma_f32_16x16x32_bf16 v[114:117], v[224:227], v[168:171], v[114:117]
	v_mfma_f32_16x16x32_bf16 v[106:109], v[216:219], v[176:179], v[106:109]
	v_mfma_f32_16x16x32_bf16 v[98:101], v[224:227], v[176:179], v[98:101]
	v_mfma_f32_16x16x32_bf16 v[90:93], v[216:219], v[184:187], v[90:93]
	v_mfma_f32_16x16x32_bf16 v[82:85], v[224:227], v[184:187], v[82:85]
	v_mfma_f32_16x16x32_bf16 v[74:77], v[216:219], v[192:195], v[74:77]
	v_mfma_f32_16x16x32_bf16 v[66:69], v[224:227], v[192:195], v[66:69]
	v_mfma_f32_16x16x32_bf16 v[122:125], v[220:223], v[172:175], v[122:125]
	v_mfma_f32_16x16x32_bf16 v[114:117], v[228:231], v[172:175], v[114:117]
	v_mfma_f32_16x16x32_bf16 v[106:109], v[220:223], v[180:183], v[106:109]
	v_mfma_f32_16x16x32_bf16 v[98:101], v[228:231], v[180:183], v[98:101]
	v_mfma_f32_16x16x32_bf16 v[90:93], v[220:223], v[188:191], v[90:93]
	v_mfma_f32_16x16x32_bf16 v[82:85], v[228:231], v[188:191], v[82:85]
	v_mfma_f32_16x16x32_bf16 v[74:77], v[220:223], v[196:199], v[74:77]
	v_mfma_f32_16x16x32_bf16 v[66:69], v[228:231], v[196:199], v[66:69]
	s_setprio 0
	s_mov_b32 m0, s81
	v_lshl_add_u64 v[162:163], v[232:233], 0, s[18:19]
	s_barrier
	ds_read_b128 v[168:171], v167 offset:49152
	ds_read_b128 v[172:175], v167 offset:50176
	ds_read_b128 v[176:179], v167 offset:51200
	ds_read_b128 v[180:183], v167 offset:52224
	ds_read_b128 v[184:187], v167 offset:53248
	ds_read_b128 v[188:191], v167 offset:54272
	ds_read_b128 v[192:195], v167 offset:55296
	ds_read_b128 v[196:199], v167 offset:56320
	global_load_lds_dwordx4 v[162:163], off
	v_lshl_add_u64 v[162:163], v[234:235], 0, s[18:19]
	s_mov_b32 m0, s82
	s_nop 0
	global_load_lds_dwordx4 v[162:163], off
	s_barrier
	s_waitcnt lgkmcnt(0)
	s_setprio 1
	s_waitcnt lgkmcnt(0)
	v_mfma_f32_16x16x32_bf16 v[62:65], v[130:133], v[168:171], v[62:65]
	v_mfma_f32_16x16x32_bf16 v[54:57], v[154:157], v[168:171], v[54:57]
	v_mfma_f32_16x16x32_bf16 v[46:49], v[130:133], v[176:179], v[46:49]
	v_mfma_f32_16x16x32_bf16 v[38:41], v[154:157], v[176:179], v[38:41]
	v_mfma_f32_16x16x32_bf16 v[30:33], v[130:133], v[184:187], v[30:33]
	v_mfma_f32_16x16x32_bf16 v[22:25], v[154:157], v[184:187], v[22:25]
	v_mfma_f32_16x16x32_bf16 v[10:13], v[130:133], v[192:195], v[10:13]
	v_mfma_f32_16x16x32_bf16 v[2:5], v[154:157], v[192:195], v[2:5]
	v_mfma_f32_16x16x32_bf16 v[62:65], v[134:137], v[172:175], v[62:65]
	v_mfma_f32_16x16x32_bf16 v[54:57], v[158:161], v[172:175], v[54:57]
	v_mfma_f32_16x16x32_bf16 v[46:49], v[134:137], v[180:183], v[46:49]
	v_mfma_f32_16x16x32_bf16 v[38:41], v[158:161], v[180:183], v[38:41]
	v_mfma_f32_16x16x32_bf16 v[30:33], v[134:137], v[188:191], v[30:33]
	v_mfma_f32_16x16x32_bf16 v[22:25], v[158:161], v[188:191], v[22:25]
	v_mfma_f32_16x16x32_bf16 v[10:13], v[134:137], v[196:199], v[10:13]
	v_mfma_f32_16x16x32_bf16 v[2:5], v[158:161], v[196:199], v[2:5]
	s_setprio 0
	s_barrier
	s_add_u32 s0, s38, 0x40080
	s_addc_u32 s1, s39, 0
	s_add_i32 s38, s42, s65
	v_lshl_add_u64 v[130:131], s[0:1], 0, v[0:1]
	s_mov_b32 m0, s38
	s_nop 0
	global_load_lds_dwordx4 v[130:131], off
	v_lshl_add_u64 v[130:131], s[0:1], 0, v[140:141]
	s_add_i32 m0, s38, 0x2000
	s_nop 0
	global_load_lds_dwordx4 v[130:131], off
	s_waitcnt vmcnt(6)
	s_barrier
	s_setprio 1
	v_mfma_f32_16x16x32_bf16 v[58:61], v[216:219], v[168:171], v[58:61]
	v_mfma_f32_16x16x32_bf16 v[50:53], v[224:227], v[168:171], v[50:53]
	v_mfma_f32_16x16x32_bf16 v[42:45], v[216:219], v[176:179], v[42:45]
	v_mfma_f32_16x16x32_bf16 v[34:37], v[224:227], v[176:179], v[34:37]
	v_mfma_f32_16x16x32_bf16 v[26:29], v[216:219], v[184:187], v[26:29]
	v_mfma_f32_16x16x32_bf16 v[18:21], v[224:227], v[184:187], v[18:21]
	v_mfma_f32_16x16x32_bf16 v[14:17], v[216:219], v[192:195], v[14:17]
	v_mfma_f32_16x16x32_bf16 v[6:9], v[224:227], v[192:195], v[6:9]
	v_mfma_f32_16x16x32_bf16 v[58:61], v[220:223], v[172:175], v[58:61]
	v_mfma_f32_16x16x32_bf16 v[50:53], v[228:231], v[172:175], v[50:53]
	v_mfma_f32_16x16x32_bf16 v[42:45], v[220:223], v[180:183], v[42:45]
	v_mfma_f32_16x16x32_bf16 v[34:37], v[228:231], v[180:183], v[34:37]
	v_mfma_f32_16x16x32_bf16 v[26:29], v[220:223], v[188:191], v[26:29]
	v_mfma_f32_16x16x32_bf16 v[18:21], v[228:231], v[188:191], v[18:21]
	v_mfma_f32_16x16x32_bf16 v[14:17], v[220:223], v[196:199], v[14:17]
	v_mfma_f32_16x16x32_bf16 v[6:9], v[228:231], v[196:199], v[6:9]
	s_setprio 0
	s_add_i32 s47, s47, 2
	s_add_u32 s3, s3, 0x100
	s_addc_u32 s14, s14, 0
	s_cmp_gt_u32 s47, 13
	s_mov_b64 s[0:1], s[12:13]
	s_barrier
	s_cbranch_scc0 .LBB0_487
;     __device__ __forceinline__ void operator()(const f32x4 (&acc)[2][2][4][2], const g8::Unit& u, int wr, int wc, int fr_, int fq_) const {
;         int fr = fr_, fq = fq_; asm volatile("" : "+v"(fr), "+v"(fq));
;         const int pn = u.pn; const int colp = pn * 256 + wc * 32 + fq * 8;
;         bf16_t* qb = (bf16_t*)(ws + AB_QB); bf16_t* kb = (bf16_t*)(ws + AB_KB); bf16_t* vT = (bf16_t*)(ws + AB_VT); bf16_t* rqb = (bf16_t*)(ws + AB_RQB); bf16_t* rkb = (bf16_t*)(ws + AB_RKB);
;         bf16_t* rkdT = (bf16_t*)(ws + AB_RKDT); bf16_t* rvT = (bf16_t*)(ws + AB_RVT); bf16_t* rgb = (bf16_t*)(ws + AB_RGB);
;         const float frqA0 = exp2f(-(float)(fq * 8) * (13.287712379549449f / 32.f)) * 0.15915494309189535f;
;         const float frqR0 = exp2f(-(float)((wc & 1) * 32 + fq * 8) * (13.287712379549449f / 63.f)) * 0.15915494309189535f;
;         constexpr float RA[8] = {1.f, 0.7498942093324559f, 0.5623413251903491f, 0.4216965034285822f, 0.31622776601683794f, 0.23713737056616552f, 0.1778279410038923f, 0.1333521432163324f};
;         constexpr float RR[8] = {1.f, 0.8639884494839686f, 0.746476040841712f, 0.6449466771037624f, 0.5572264795507174f, 0.4814372420784346f, 0.4159562163071847f, 0.35938136638046275f};
; #pragma unroll
;         for (int ai = 0; ai < 2; ++ai)
; #pragma unroll
;             for (int m = 0; m < 4; ++m) {
;                 const int t = u.pm * 256 + ai * 128 + wr * 64 + m * 16 + fr, sq = t & (SEQ - 1), b = t >> 13;
;                 f32x4 x[2][2];
; #pragma unroll
;                 for (int bj = 0; bj < 2; ++bj)
; #pragma unroll
;                     for (int n = 0; n < 2; ++n) x[bj][n] = acc[ai][bj][m][n];
;                 if (pn < 4 || (pn == 4 && wc < 2)) {
;                     const int j0 = fq * 8; const float sc = pn < 4 ? 0.125f : 1.f;
;                     u32x4 w1, w2;
; #pragma unroll
;                     for (int n = 0; n < 2; ++n) { f32x4 o1, o2;
; #pragma unroll
;                         for (int e = 0; e < 4; ++e) { const float rev = __builtin_amdgcn_fractf((float)sq * (frqA0 * RA[4 * n + e])); const float cc = __builtin_amdgcn_cosf(rev) * sc, ss = __builtin_amdgcn_sinf(rev) * sc;
;                             o1[e] = x[0][n][e] * cc - x[1][n][e] * ss; o2[e] = x[1][n][e] * cc + x[0][n][e] * ss; }
	s_nop 0
	s_nop 0
	s_nop 0
	s_nop 0
	s_nop 0
	s_nop 0
	s_nop 0
	s_nop 0
	s_nop 0
	s_nop 0
	s_lshl_b32 s2, s2, 8
	s_add_i32 s2, s2, s80
	s_cmp_lt_i32 s94, 4
	s_cselect_b64 s[36:37], -1, 0
	s_cmp_lg_u32 s94, 4
	v_mov_b32_e32 v131, v164
	v_mov_b32_e32 v130, v139
	s_cselect_b64 s[12:13], -1, 0
	s_cmp_eq_u32 s94, 4
	s_nop 0
	v_add_u32_e32 v160, s2, v131
	s_cselect_b64 s[2:3], -1, 0
	s_and_b64 s[2:3], s[2:3], s[10:11]
	s_cmp_gt_u32 s94, 8
	s_cselect_b64 s[56:57], -1, 0
	s_cmp_gt_u32 s94, 12
	s_cselect_b64 s[54:55], -1, 0
	s_lshl_b32 s42, s94, 8
	s_add_i32 s14, s42, 0xfffff300
	v_lshlrev_b32_e32 v130, 3, v130
	s_lshl_b64 s[22:23], s[14:15], 1
	v_add_u32_e32 v132, s85, v130
	s_add_u32 s22, s87, s22
	v_cvt_f32_i32_e32 v133, v132
	s_addc_u32 s23, s88, s23
	s_add_i32 s14, s86, s42
	s_cmp_gt_u32 s94, 6
	v_add_u32_e32 v171, s14, v130
	s_cselect_b64 s[38:39], -1, 0
	s_lshl_b32 s14, s94, 1
	s_and_b32 s14, s14, 2
	v_mul_f32_e32 v134, 0xbe57fa62, v133
	s_or_b32 s14, s14, s89
	v_cmp_gt_f32_e32 vcc, s66, v134
	v_ashrrev_i32_e32 v131, 31, v130
	s_lshl_b32 s14, s14, 7
	v_cvt_f32_i32_e32 v172, v130
	v_cndmask_b32_e32 v134, 0, v207, vcc
	v_lshlrev_b64 v[162:163], 1, v[130:131]
	s_xor_b32 s14, s14, 0x100
	v_fmac_f32_e32 v134, 0xbe57fa62, v133
	v_lshl_add_u64 v[158:159], s[22:23], 0, v[162:163]
	s_and_b64 s[22:23], s[38:39], exec
	v_exp_f32_e32 v133, v134
	s_mov_b32 s22, 0x3d420000
	s_cselect_b32 s22, s22, 0x3c420000
	v_mul_f32_e32 v134, 0xbed49a78, v172
	s_add_u32 s22, s40, s22
	v_cmp_gt_f32_e64 s[0:1], s66, v134
	v_cndmask_b32_e32 v134, 0, v208, vcc
	v_add_u32_e32 v170, s14, v132
	s_addc_u32 s23, s41, 0
	s_lshl_b32 s14, s14, 1
	v_ldexp_f32 v133, v133, v134
	s_add_u32 s22, s22, s14
	v_mul_f32_e32 v169, 0.15915494, v133
	s_addc_u32 s23, s23, 0
	v_ashrrev_i32_e32 v133, 31, v132
	v_lshl_add_u64 v[154:155], v[132:133], 1, s[22:23]
	s_or_b32 s22, s42, s75
	s_ashr_i32 s23, s22, 31
	s_lshl_b64 s[22:23], s[22:23], 1
	s_add_u32 s42, s83, s22
	v_mov_b32_e32 v131, 0x3db504f3
	s_addc_u32 s43, s84, s23
	s_nor_b64 s[22:23], s[36:37], s[2:3]
	v_cndmask_b32_e64 v156, 1.0, v131, s[38:39]
	v_add_u32_e32 v168, s90, v130
	v_and_b32_e32 v173, 0x1fff, v160
	s_mov_b64 s[2:3], -1
	s_and_b64 vcc, exec, s[22:23]
	s_cbranch_vccz .LBB0_506
	v_ashrrev_i32_e32 v174, 13, v160
	s_and_b64 vcc, exec, s[12:13]
	s_cbranch_vccz .LBB0_503
	s_and_b64 vcc, exec, s[56:57]
	s_cbranch_vccz .LBB0_496
	s_andn2_b64 vcc, exec, s[54:55]
	s_cbranch_vccnz .LBB0_493
	v_mul_f32_e32 v132, 0xbfb8aa3b, v126
	v_mul_f32_e32 v133, 0xbfb8aa3b, v127
	v_mul_f32_e32 v134, 0xbfb8aa3b, v128
	v_mul_f32_e32 v135, 0xbfb8aa3b, v129
	v_exp_f32_e32 v132, v132
	v_exp_f32_e32 v133, v133
	v_exp_f32_e32 v134, v134
	v_exp_f32_e32 v135, v135
	v_mul_f32_e32 v136, 0xbfb8aa3b, v120
	v_pk_add_f32 v[132:133], v[132:133], 1.0 op_sel_hi:[1,0]
	v_mul_f32_e32 v137, 0xbfb8aa3b, v121
	v_pk_add_f32 v[134:135], v[134:135], 1.0 op_sel_hi:[1,0]
	v_rcp_f32_e32 v132, v132
	v_rcp_f32_e32 v133, v133
	v_rcp_f32_e32 v134, v134
	v_rcp_f32_e32 v135, v135
	v_exp_f32_e32 v136, v136
	v_pk_mul_f32 v[132:133], v[126:127], v[132:133]
	v_exp_f32_e32 v137, v137
	v_pk_mul_f32 v[134:135], v[128:129], v[134:135]
	v_cvt_pk_bf16_f32 v132, v132, v133
	v_ashrrev_i32_e32 v161, 31, v160
	v_cvt_pk_bf16_f32 v133, v134, v135
	v_mul_f32_e32 v134, 0xbfb8aa3b, v118
	v_mul_f32_e32 v135, 0xbfb8aa3b, v119
	v_exp_f32_e32 v134, v134
	v_exp_f32_e32 v135, v135
	v_pk_add_f32 v[136:137], v[136:137], 1.0 op_sel_hi:[1,0]
	v_lshlrev_b64 v[130:131], 11, v[160:161]
	v_rcp_f32_e32 v136, v136
	v_pk_add_f32 v[134:135], v[134:135], 1.0 op_sel_hi:[1,0]
	v_rcp_f32_e32 v137, v137
	v_rcp_f32_e32 v134, v134
	v_rcp_f32_e32 v135, v135
	v_lshl_add_u64 v[130:131], v[158:159], 0, v[130:131]
	v_pk_mul_f32 v[136:137], v[120:121], v[136:137]
	s_mov_b64 s[2:3], 0
	v_pk_mul_f32 v[134:135], v[118:119], v[134:135]
	s_nop 0
	v_cvt_pk_bf16_f32 v134, v134, v135
	v_cvt_pk_bf16_f32 v135, v136, v137
	global_store_dwordx4 v[130:131], v[132:135], off
	v_mul_f32_e32 v136, 0xbfb8aa3b, v116
	v_mul_f32_e32 v137, 0xbfb8aa3b, v117
	v_mul_f32_e32 v132, 0xbfb8aa3b, v122
	v_mul_f32_e32 v133, 0xbfb8aa3b, v123
	v_mul_f32_e32 v134, 0xbfb8aa3b, v124
	v_mul_f32_e32 v135, 0xbfb8aa3b, v125
	v_exp_f32_e32 v132, v132
	v_exp_f32_e32 v133, v133
	v_exp_f32_e32 v134, v134
	v_exp_f32_e32 v135, v135
	v_exp_f32_e32 v136, v136
	v_pk_add_f32 v[132:133], v[132:133], 1.0 op_sel_hi:[1,0]
	v_exp_f32_e32 v137, v137
	v_pk_add_f32 v[134:135], v[134:135], 1.0 op_sel_hi:[1,0]
	v_rcp_f32_e32 v132, v132
	v_rcp_f32_e32 v133, v133
	v_rcp_f32_e32 v134, v134
	v_rcp_f32_e32 v135, v135
	v_pk_add_f32 v[136:137], v[136:137], 1.0 op_sel_hi:[1,0]
	v_pk_mul_f32 v[132:133], v[122:123], v[132:133]
	v_rcp_f32_e32 v136, v136
	v_pk_mul_f32 v[134:135], v[124:125], v[134:135]
	v_cvt_pk_bf16_f32 v132, v132, v133
	v_rcp_f32_e32 v137, v137
	v_cvt_pk_bf16_f32 v133, v134, v135
	v_mul_f32_e32 v134, 0xbfb8aa3b, v114
	v_mul_f32_e32 v135, 0xbfb8aa3b, v115
	v_exp_f32_e32 v134, v134
	v_exp_f32_e32 v135, v135
	v_pk_mul_f32 v[136:137], v[116:117], v[136:137]
	v_pk_add_f32 v[134:135], v[134:135], 1.0 op_sel_hi:[1,0]
	s_nop 0
	v_rcp_f32_e32 v134, v134
	v_rcp_f32_e32 v135, v135
	s_nop 0
	v_pk_mul_f32 v[134:135], v[114:115], v[134:135]
	s_nop 0
	v_cvt_pk_bf16_f32 v134, v134, v135
	v_cvt_pk_bf16_f32 v135, v136, v137
	global_store_dwordx4 v[130:131], v[132:135], off offset:256

; #define G8_STAGE(bufoff, gbase, voff) do { _Pragma("unroll") for (int _i = 0; _i < 2; ++_i) \
;         __builtin_amdgcn_global_load_lds((const unsigned*)((const char*)(gbase) + (voff)[_i]), (LAS unsigned*)(lds + (bufoff) + ldsw + _i * 8192), 16, 0, 0); } while (0)
; #define G8_LDA(dst, b, h) do { _Pragma("unroll") for (int m = 0; m < 4; ++m) _Pragma("unroll") for (int k = 0; k < 2; ++k) dst[m][k] = *(const LAS bf16x8*)(lds + G8_SA(b, h) + aoff + m * 2048 + k * 1024); } while (0)
; #define G8_LDB(dst, b, h) do { _Pragma("unroll") for (int n = 0; n < 2; ++n) _Pragma("unroll") for (int k = 0; k < 2; ++k) dst[n][k] = *(const LAS bf16x8*)(lds + G8_SB(b, h) + boff + n * 2048 + k * 1024); } while (0)
; #define G8_MMA(ai, bj, At, Bt) do { __builtin_amdgcn_s_setprio(1); _Pragma("unroll") for (int m = 0; m < 4; ++m) _Pragma("unroll") for (int n = 0; n < 2; ++n) _Pragma("unroll") for (int k = 0; k < 2; ++k) \
;         acc[ai][bj][m][n] = __builtin_amdgcn_mfma_f32_16x16x32_bf16(Bt[n][k], At[m][k], acc[ai][bj][m][n], 0, 0, 0); __builtin_amdgcn_s_setprio(0); } while (0)
; #define G8_WAIT_L(n) asm volatile("s_waitcnt lgkmcnt(" #n ")" ::: "memory")
; #define G8_BAR __builtin_amdgcn_s_barrier()
;     __device__ __forceinline__ void init(f32x4 (&acc)[2][2][4][2], const Unit& u, int wc, int fq) const {
;         const int col0 = u.pn * BM + wc * 32 + 8 * fq;
; #pragma unroll
;         for (int b = 0; b < 2; ++b)
; #pragma unroll
;             for (int n = 0; n < 2; ++n) { const f32x4 bv = *(const f32x4*)(bias + col0 + b * HALF + 4 * n);
; #pragma unroll
;                 for (int a = 0; a < 2; ++a)
; #pragma unroll
;                     for (int m = 0; m < 4; ++m) acc[a][b][m][n] = bv; } }
; template <class Epi, class Sched>
; __device__ __forceinline__ void gemm_phase(LAS unsigned char* lds, const int K, const Sched& S, const Epi& E) {
;     ...
;             G8_LDB(B0, 0, 0); G8_SCHED; G8_LDA(At, 0, 0); G8_STAGE(G8_SA(1, 1), a1, oc[1]);
;             if (last && has_next) S.aoff(nxt, tid, oc);
;             G8_WAIT_L(8); G8_BAR; G8_WAIT_L(0); G8_MMA(0, 0, At, B0); G8_BAR; G8_SCHED;
;             G8_LDB(B1, 0, 1); G8_STAGE(G8_SB(0, 0), b2, voffB);
;             G8_BAR; G8_WAIT_L(0); G8_MMA(0, 1, At, B1); G8_BAR;
;             G8_LDA(At, 0, 1); G8_STAGE(G8_SA(0, 0), a2, oc[0]);
;             G8_BAR; G8_WAIT_L(0); G8_MMA(1, 0, At, B0); G8_BAR; G8_SCHED;
.LBB0_2251:
	s_add_u32 s12, s12, 0x80
	v_mov_b64_e32 v[18:19], 0x100
	s_addc_u32 s13, s13, 0
	v_cmp_lt_i64_e32 vcc, s[24:25], v[18:19]
	s_add_u32 s58, s22, 0x100
	s_waitcnt vmcnt(0)
	v_mov_b64_e32 v[20:21], v[4:5]
	v_mov_b64_e32 v[24:25], v[8:9]
	v_mov_b64_e32 v[36:37], v[4:5]
	v_mov_b64_e32 v[40:41], v[8:9]
	v_mov_b64_e32 v[52:53], v[4:5]
	v_mov_b64_e32 v[56:57], v[8:9]
	v_mov_b64_e32 v[28:29], v[12:13]
	v_mov_b64_e32 v[32:33], v[16:17]
	v_mov_b64_e32 v[44:45], v[12:13]
	v_mov_b64_e32 v[48:49], v[16:17]
	v_mov_b64_e32 v[60:61], v[12:13]
	v_mov_b64_e32 v[64:65], v[16:17]
	v_mov_b64_e32 v[68:69], v[4:5]
	v_mov_b64_e32 v[72:73], v[8:9]
	v_mov_b64_e32 v[84:85], v[4:5]
	v_mov_b64_e32 v[88:89], v[8:9]
	v_mov_b64_e32 v[100:101], v[4:5]
	v_mov_b64_e32 v[104:105], v[8:9]
	v_mov_b64_e32 v[116:117], v[4:5]
	v_mov_b64_e32 v[120:121], v[8:9]
	v_mov_b64_e32 v[76:77], v[12:13]
	v_mov_b64_e32 v[80:81], v[16:17]
	v_mov_b64_e32 v[92:93], v[12:13]
	v_mov_b64_e32 v[96:97], v[16:17]
	v_mov_b64_e32 v[108:109], v[12:13]
	v_mov_b64_e32 v[112:113], v[16:17]
	v_mov_b64_e32 v[124:125], v[12:13]
	v_mov_b64_e32 v[128:129], v[16:17]
	s_addc_u32 s59, s23, 0
	s_mov_b32 s22, 0
	v_mov_b64_e32 v[18:19], v[2:3]
	v_mov_b64_e32 v[22:23], v[6:7]
	v_mov_b64_e32 v[34:35], v[2:3]
	v_mov_b64_e32 v[38:39], v[6:7]
	v_mov_b64_e32 v[50:51], v[2:3]
	v_mov_b64_e32 v[54:55], v[6:7]
	v_mov_b64_e32 v[26:27], v[10:11]
	v_mov_b64_e32 v[30:31], v[14:15]
	v_mov_b64_e32 v[42:43], v[10:11]
	v_mov_b64_e32 v[46:47], v[14:15]
	v_mov_b64_e32 v[58:59], v[10:11]
	v_mov_b64_e32 v[62:63], v[14:15]
	v_mov_b64_e32 v[66:67], v[2:3]
	v_mov_b64_e32 v[70:71], v[6:7]
	v_mov_b64_e32 v[82:83], v[2:3]
	v_mov_b64_e32 v[86:87], v[6:7]
	v_mov_b64_e32 v[98:99], v[2:3]
	v_mov_b64_e32 v[102:103], v[6:7]
	v_mov_b64_e32 v[114:115], v[2:3]
	v_mov_b64_e32 v[118:119], v[6:7]
	v_mov_b64_e32 v[74:75], v[10:11]
	v_mov_b64_e32 v[78:79], v[14:15]
	v_mov_b64_e32 v[90:91], v[10:11]
	v_mov_b64_e32 v[94:95], v[14:15]
	v_mov_b64_e32 v[106:107], v[10:11]
	v_mov_b64_e32 v[110:111], v[14:15]
	v_mov_b64_e32 v[122:123], v[10:11]
	v_mov_b64_e32 v[126:127], v[14:15]
	s_nop 0
	s_nop 0
	s_nop 0
	s_nop 0
	s_nop 0
	s_nop 0
	s_nop 0
.LBB0_2252:
	s_add_i32 s60, s22, 2
	s_add_u32 s24, s12, 0x80
	s_addc_u32 s23, s13, 0
	s_add_i32 s61, 0, 0x10000
	v_add_u32_e32 v144, s61, v148
	ds_read_b128 v[152:155], v144
	ds_read_b128 v[156:159], v144 offset:1024
	ds_read_b128 v[160:163], v144 offset:2048
	ds_read_b128 v[164:167], v144 offset:3072
	s_cmp_eq_u32 s51, s22
	s_cselect_b32 s22, s0, s24
	s_cselect_b32 s23, s1, s23
	s_cselect_b32 s25, s11, s59
	s_cselect_b32 s24, s10, s58
	v_lshl_add_u64 v[144:145], s[12:13], 0, v[140:141]
	s_add_i32 m0, s44, 0xc000
	ds_read_b128 v[168:171], v150
	ds_read_b128 v[172:175], v150 offset:1024
	ds_read_b128 v[176:179], v150 offset:2048
	ds_read_b128 v[180:183], v150 offset:3072
	ds_read_b128 v[184:187], v150 offset:4096
	ds_read_b128 v[188:191], v150 offset:5120
	ds_read_b128 v[192:195], v150 offset:6144
	ds_read_b128 v[196:199], v150 offset:7168
	global_load_lds_dwordx4 v[144:145], off
	v_lshl_add_u64 v[144:145], s[12:13], 0, v[142:143]
	s_add_i32 m0, s44, 0xe000
	s_nop 0
	global_load_lds_dwordx4 v[144:145], off
	s_waitcnt lgkmcnt(8)
	s_barrier
	s_waitcnt lgkmcnt(0)
	s_setprio 1
	s_waitcnt lgkmcnt(0)
	v_mfma_f32_16x16x32_bf16 v[126:129], v[152:155], v[168:171], v[126:129]
	v_mfma_f32_16x16x32_bf16 v[122:125], v[160:163], v[168:171], v[122:125]
	v_mfma_f32_16x16x32_bf16 v[110:113], v[152:155], v[176:179], v[110:113]
	v_mfma_f32_16x16x32_bf16 v[106:109], v[160:163], v[176:179], v[106:109]
	v_mfma_f32_16x16x32_bf16 v[94:97], v[152:155], v[184:187], v[94:97]
	v_mfma_f32_16x16x32_bf16 v[90:93], v[160:163], v[184:187], v[90:93]
	v_mfma_f32_16x16x32_bf16 v[78:81], v[152:155], v[192:195], v[78:81]
	v_mfma_f32_16x16x32_bf16 v[74:77], v[160:163], v[192:195], v[74:77]
	v_mfma_f32_16x16x32_bf16 v[126:129], v[156:159], v[172:175], v[126:129]
	v_mfma_f32_16x16x32_bf16 v[122:125], v[164:167], v[172:175], v[122:125]
	v_mfma_f32_16x16x32_bf16 v[110:113], v[156:159], v[180:183], v[110:113]
	v_mfma_f32_16x16x32_bf16 v[106:109], v[164:167], v[180:183], v[106:109]
	v_mfma_f32_16x16x32_bf16 v[94:97], v[156:159], v[188:191], v[94:97]
	v_mfma_f32_16x16x32_bf16 v[90:93], v[164:167], v[188:191], v[90:93]
	v_mfma_f32_16x16x32_bf16 v[78:81], v[156:159], v[196:199], v[78:81]
	v_mfma_f32_16x16x32_bf16 v[74:77], v[164:167], v[196:199], v[74:77]
	s_setprio 0
	s_barrier
	s_add_i32 s62, 0, 0x14000
	v_add_u32_e32 v144, s62, v148
	s_add_i32 s61, s61, s43
	ds_read_b128 v[216:219], v144
	ds_read_b128 v[220:223], v144 offset:1024
	ds_read_b128 v[224:227], v144 offset:2048
	ds_read_b128 v[228:231], v144 offset:3072
	v_lshl_add_u64 v[144:145], s[24:25], 0, v[0:1]
	s_mov_b32 m0, s61
	v_lshl_add_u64 v[200:201], s[24:25], 0, v[130:131]
	global_load_lds_dwordx4 v[144:145], off
	s_add_i32 m0, s61, 0x2000
	s_nop 0
	global_load_lds_dwordx4 v[200:201], off
	s_barrier
	s_waitcnt lgkmcnt(0)
	s_setprio 1
	s_waitcnt lgkmcnt(0)
	v_mfma_f32_16x16x32_bf16 v[118:121], v[216:219], v[168:171], v[118:121]
	v_mfma_f32_16x16x32_bf16 v[114:117], v[224:227], v[168:171], v[114:117]
	v_mfma_f32_16x16x32_bf16 v[102:105], v[216:219], v[176:179], v[102:105]
	v_mfma_f32_16x16x32_bf16 v[98:101], v[224:227], v[176:179], v[98:101]
	v_mfma_f32_16x16x32_bf16 v[86:89], v[216:219], v[184:187], v[86:89]
	v_mfma_f32_16x16x32_bf16 v[82:85], v[224:227], v[184:187], v[82:85]
	v_mfma_f32_16x16x32_bf16 v[70:73], v[216:219], v[192:195], v[70:73]
	v_mfma_f32_16x16x32_bf16 v[66:69], v[224:227], v[192:195], v[66:69]
	v_mfma_f32_16x16x32_bf16 v[118:121], v[220:223], v[172:175], v[118:121]
	v_mfma_f32_16x16x32_bf16 v[114:117], v[228:231], v[172:175], v[114:117]
	v_mfma_f32_16x16x32_bf16 v[102:105], v[220:223], v[180:183], v[102:105]
	v_mfma_f32_16x16x32_bf16 v[98:101], v[228:231], v[180:183], v[98:101]
	v_mfma_f32_16x16x32_bf16 v[86:89], v[220:223], v[188:191], v[86:89]
	v_mfma_f32_16x16x32_bf16 v[82:85], v[228:231], v[188:191], v[82:85]
	v_mfma_f32_16x16x32_bf16 v[70:73], v[220:223], v[196:199], v[70:73]
	v_mfma_f32_16x16x32_bf16 v[66:69], v[228:231], v[196:199], v[66:69]
	s_setprio 0
	s_mov_b32 m0, s44
	v_lshl_add_u64 v[232:233], s[22:23], 0, v[132:133]
	s_barrier
; #define G8_STAGE(bufoff, gbase, voff) do { _Pragma("unroll") for (int _i = 0; _i < 2; ++_i) \
;         __builtin_amdgcn_global_load_lds((const unsigned*)((const char*)(gbase) + (voff)[_i]), (LAS unsigned*)(lds + (bufoff) + ldsw + _i * 8192), 16, 0, 0); } while (0)
; #define G8_LDA(dst, b, h) do { _Pragma("unroll") for (int m = 0; m < 4; ++m) _Pragma("unroll") for (int k = 0; k < 2; ++k) dst[m][k] = *(const LAS bf16x8*)(lds + G8_SA(b, h) + aoff + m * 2048 + k * 1024); } while (0)
; #define G8_LDB(dst, b, h) do { _Pragma("unroll") for (int n = 0; n < 2; ++n) _Pragma("unroll") for (int k = 0; k < 2; ++k) dst[n][k] = *(const LAS bf16x8*)(lds + G8_SB(b, h) + boff + n * 2048 + k * 1024); } while (0)
; #define G8_MMA(ai, bj, At, Bt) do { __builtin_amdgcn_s_setprio(1); _Pragma("unroll") for (int m = 0; m < 4; ++m) _Pragma("unroll") for (int n = 0; n < 2; ++n) _Pragma("unroll") for (int k = 0; k < 2; ++k) \
;         acc[ai][bj][m][n] = __builtin_amdgcn_mfma_f32_16x16x32_bf16(Bt[n][k], At[m][k], acc[ai][bj][m][n], 0, 0, 0); __builtin_amdgcn_s_setprio(0); } while (0)
; #define G8_WAIT_V(n) asm volatile("s_waitcnt vmcnt(" #n ")" ::: "memory")
; #define G8_WAIT_L(n) asm volatile("s_waitcnt lgkmcnt(" #n ")" ::: "memory")
; #define G8_BAR __builtin_amdgcn_s_barrier()
; #define G8_SCHED __builtin_amdgcn_sched_barrier(0)
; template <class Epi, class Sched>
; __device__ __forceinline__ void gemm_phase(LAS unsigned char* lds, const int K, const Sched& S, const Epi& E) {
;     ...
;             G8_BAR; G8_WAIT_L(0); G8_MMA(0, 1, At, B1); G8_BAR;
;             G8_LDA(At, 0, 1); G8_STAGE(G8_SA(0, 0), a2, oc[0]);
;             G8_BAR; G8_WAIT_L(0); G8_MMA(1, 0, At, B0); G8_BAR; G8_SCHED;
;             G8_STAGE(G8_SB(0, 1), b2 + hstep, voffB);
;             G8_WAIT_V(6); G8_BAR; G8_MMA(1, 1, At, B1); G8_BAR;
;             G8_LDB(B0, 1, 0); G8_SCHED; G8_LDA(At, 1, 0); G8_STAGE(G8_SA(0, 1), a2, oc[1]);
;             G8_WAIT_L(8); G8_BAR; G8_WAIT_L(0); G8_MMA(0, 0, At, B0); G8_BAR; G8_SCHED;
;             G8_LDB(B1, 1, 1); G8_STAGE(G8_SB(1, 0), b3, voffB);
;             G8_BAR; G8_WAIT_L(0); G8_MMA(0, 1, At, B1); G8_BAR;
;             G8_LDA(At, 1, 1); G8_STAGE(G8_SA(1, 0), a3, oc[0]);
;             G8_BAR; G8_WAIT_L(0); G8_MMA(1, 0, At, B0); G8_BAR; G8_SCHED;
	ds_read_b128 v[168:171], v150 offset:16384
	ds_read_b128 v[172:175], v150 offset:17408
	ds_read_b128 v[176:179], v150 offset:18432
	ds_read_b128 v[180:183], v150 offset:19456
	ds_read_b128 v[184:187], v150 offset:20480
	ds_read_b128 v[188:191], v150 offset:21504
	ds_read_b128 v[192:195], v150 offset:22528
	ds_read_b128 v[196:199], v150 offset:23552
	global_load_lds_dwordx4 v[232:233], off
	v_lshl_add_u64 v[234:235], s[22:23], 0, v[136:137]
	s_mov_b32 m0, s45
	s_nop 0
	global_load_lds_dwordx4 v[234:235], off
	s_barrier
	s_waitcnt lgkmcnt(0)
	s_setprio 1
	s_waitcnt lgkmcnt(0)
	v_mfma_f32_16x16x32_bf16 v[62:65], v[152:155], v[168:171], v[62:65]
	v_mfma_f32_16x16x32_bf16 v[58:61], v[160:163], v[168:171], v[58:61]
	v_mfma_f32_16x16x32_bf16 v[46:49], v[152:155], v[176:179], v[46:49]
	v_mfma_f32_16x16x32_bf16 v[42:45], v[160:163], v[176:179], v[42:45]
	v_mfma_f32_16x16x32_bf16 v[30:33], v[152:155], v[184:187], v[30:33]
	v_mfma_f32_16x16x32_bf16 v[26:29], v[160:163], v[184:187], v[26:29]
	v_mfma_f32_16x16x32_bf16 v[14:17], v[152:155], v[192:195], v[14:17]
	v_mfma_f32_16x16x32_bf16 v[10:13], v[160:163], v[192:195], v[10:13]
	v_mfma_f32_16x16x32_bf16 v[62:65], v[156:159], v[172:175], v[62:65]
	v_mfma_f32_16x16x32_bf16 v[58:61], v[164:167], v[172:175], v[58:61]
	v_mfma_f32_16x16x32_bf16 v[46:49], v[156:159], v[180:183], v[46:49]
	v_mfma_f32_16x16x32_bf16 v[42:45], v[164:167], v[180:183], v[42:45]
	v_mfma_f32_16x16x32_bf16 v[30:33], v[156:159], v[188:191], v[30:33]
	v_mfma_f32_16x16x32_bf16 v[26:29], v[164:167], v[188:191], v[26:29]
	v_mfma_f32_16x16x32_bf16 v[14:17], v[156:159], v[196:199], v[14:17]
	v_mfma_f32_16x16x32_bf16 v[10:13], v[164:167], v[196:199], v[10:13]
	s_setprio 0
	s_barrier
	s_add_u32 s24, s24, s42
	s_addc_u32 s25, s25, 0
	s_add_i32 s61, s62, s43
	v_lshl_add_u64 v[236:237], s[24:25], 0, v[0:1]
	s_mov_b32 m0, s61
	v_lshl_add_u64 v[238:239], s[24:25], 0, v[130:131]
	global_load_lds_dwordx4 v[236:237], off
	s_add_i32 m0, s61, 0x2000
	s_nop 0
	global_load_lds_dwordx4 v[238:239], off
	s_waitcnt vmcnt(6)
	s_barrier
	s_setprio 1
	v_mfma_f32_16x16x32_bf16 v[54:57], v[216:219], v[168:171], v[54:57]
	v_mfma_f32_16x16x32_bf16 v[50:53], v[224:227], v[168:171], v[50:53]
	v_mfma_f32_16x16x32_bf16 v[38:41], v[216:219], v[176:179], v[38:41]
	v_mfma_f32_16x16x32_bf16 v[34:37], v[224:227], v[176:179], v[34:37]
	v_mfma_f32_16x16x32_bf16 v[22:25], v[216:219], v[184:187], v[22:25]
	v_mfma_f32_16x16x32_bf16 v[18:21], v[224:227], v[184:187], v[18:21]
	v_mfma_f32_16x16x32_bf16 v[6:9], v[216:219], v[192:195], v[6:9]
	v_mfma_f32_16x16x32_bf16 v[2:5], v[224:227], v[192:195], v[2:5]
	v_mfma_f32_16x16x32_bf16 v[54:57], v[220:223], v[172:175], v[54:57]
	v_mfma_f32_16x16x32_bf16 v[50:53], v[228:231], v[172:175], v[50:53]
	v_mfma_f32_16x16x32_bf16 v[38:41], v[220:223], v[180:183], v[38:41]
	v_mfma_f32_16x16x32_bf16 v[34:37], v[228:231], v[180:183], v[34:37]
	v_mfma_f32_16x16x32_bf16 v[22:25], v[220:223], v[188:191], v[22:25]
	v_mfma_f32_16x16x32_bf16 v[18:21], v[228:231], v[188:191], v[18:21]
	v_mfma_f32_16x16x32_bf16 v[6:9], v[220:223], v[196:199], v[6:9]
	v_mfma_f32_16x16x32_bf16 v[2:5], v[228:231], v[196:199], v[2:5]
	s_setprio 0
	s_add_i32 s24, 0, 0x18000
	v_add_u32_e32 v151, s24, v148
	s_barrier
	ds_read_b128 v[152:155], v151
	ds_read_b128 v[156:159], v151 offset:1024
	ds_read_b128 v[160:163], v151 offset:2048
	ds_read_b128 v[164:167], v151 offset:3072
	s_mov_b32 m0, s46
	v_lshl_add_u64 v[216:217], s[22:23], 0, v[134:135]
	ds_read_b128 v[168:171], v150 offset:32768
	ds_read_b128 v[172:175], v150 offset:33792
	ds_read_b128 v[176:179], v150 offset:34816
	ds_read_b128 v[180:183], v150 offset:35840
	ds_read_b128 v[184:187], v150 offset:36864
	ds_read_b128 v[188:191], v150 offset:37888
	ds_read_b128 v[192:195], v150 offset:38912
	ds_read_b128 v[196:199], v150 offset:39936
	global_load_lds_dwordx4 v[216:217], off
	v_lshl_add_u64 v[216:217], s[22:23], 0, v[138:139]
	s_mov_b32 m0, s47
	s_nop 0
	global_load_lds_dwordx4 v[216:217], off
	s_waitcnt lgkmcnt(8)
	s_barrier
	s_waitcnt lgkmcnt(0)
	s_setprio 1
	s_waitcnt lgkmcnt(0)
	v_mfma_f32_16x16x32_bf16 v[126:129], v[152:155], v[168:171], v[126:129]
	v_mfma_f32_16x16x32_bf16 v[122:125], v[160:163], v[168:171], v[122:125]
	v_mfma_f32_16x16x32_bf16 v[110:113], v[152:155], v[176:179], v[110:113]
	v_mfma_f32_16x16x32_bf16 v[106:109], v[160:163], v[176:179], v[106:109]
	v_mfma_f32_16x16x32_bf16 v[94:97], v[152:155], v[184:187], v[94:97]
	v_mfma_f32_16x16x32_bf16 v[90:93], v[160:163], v[184:187], v[90:93]
	v_mfma_f32_16x16x32_bf16 v[78:81], v[152:155], v[192:195], v[78:81]
	v_mfma_f32_16x16x32_bf16 v[74:77], v[160:163], v[192:195], v[74:77]
	v_mfma_f32_16x16x32_bf16 v[126:129], v[156:159], v[172:175], v[126:129]
	v_mfma_f32_16x16x32_bf16 v[122:125], v[164:167], v[172:175], v[122:125]
	v_mfma_f32_16x16x32_bf16 v[110:113], v[156:159], v[180:183], v[110:113]
	v_mfma_f32_16x16x32_bf16 v[106:109], v[164:167], v[180:183], v[106:109]
	v_mfma_f32_16x16x32_bf16 v[94:97], v[156:159], v[188:191], v[94:97]
	v_mfma_f32_16x16x32_bf16 v[90:93], v[164:167], v[188:191], v[90:93]
	v_mfma_f32_16x16x32_bf16 v[78:81], v[156:159], v[196:199], v[78:81]
	v_mfma_f32_16x16x32_bf16 v[74:77], v[164:167], v[196:199], v[74:77]
	s_setprio 0
	s_barrier
	s_add_i32 s22, 0, 0x1c000
	s_add_i32 s23, s24, s43
	v_add_u32_e32 v151, s22, v148
	v_lshl_add_u64 v[144:145], v[144:145], 0, s[18:19]
	s_mov_b32 m0, s23
	ds_read_b128 v[216:219], v151
	ds_read_b128 v[220:223], v151 offset:1024
	ds_read_b128 v[224:227], v151 offset:2048
	ds_read_b128 v[228:231], v151 offset:3072
	global_load_lds_dwordx4 v[144:145], off
	v_lshl_add_u64 v[144:145], v[200:201], 0, s[18:19]
	s_add_i32 m0, s23, 0x2000
	s_nop 0
	global_load_lds_dwordx4 v[144:145], off
	s_barrier
; #define G8_STAGE(bufoff, gbase, voff) do { _Pragma("unroll") for (int _i = 0; _i < 2; ++_i) \
;         __builtin_amdgcn_global_load_lds((const unsigned*)((const char*)(gbase) + (voff)[_i]), (LAS unsigned*)(lds + (bufoff) + ldsw + _i * 8192), 16, 0, 0); } while (0)
; #define G8_LDA(dst, b, h) do { _Pragma("unroll") for (int m = 0; m < 4; ++m) _Pragma("unroll") for (int k = 0; k < 2; ++k) dst[m][k] = *(const LAS bf16x8*)(lds + G8_SA(b, h) + aoff + m * 2048 + k * 1024); } while (0)
; #define G8_MMA(ai, bj, At, Bt) do { __builtin_amdgcn_s_setprio(1); _Pragma("unroll") for (int m = 0; m < 4; ++m) _Pragma("unroll") for (int n = 0; n < 2; ++n) _Pragma("unroll") for (int k = 0; k < 2; ++k) \
;         acc[ai][bj][m][n] = __builtin_amdgcn_mfma_f32_16x16x32_bf16(Bt[n][k], At[m][k], acc[ai][bj][m][n], 0, 0, 0); __builtin_amdgcn_s_setprio(0); } while (0)
; #define G8_WAIT_V(n) asm volatile("s_waitcnt vmcnt(" #n ")" ::: "memory")
; #define G8_WAIT_L(n) asm volatile("s_waitcnt lgkmcnt(" #n ")" ::: "memory")
; #define G8_BAR __builtin_amdgcn_s_barrier()
; #define G8_SCHED __builtin_amdgcn_sched_barrier(0)
; template <class Epi, class Sched>
; __device__ __forceinline__ void gemm_phase(LAS unsigned char* lds, const int K, const Sched& S, const Epi& E) {
;     ...
;             G8_BAR; G8_WAIT_L(0); G8_MMA(0, 1, At, B1); G8_BAR;
;             G8_LDA(At, 1, 1); G8_STAGE(G8_SA(1, 0), a3, oc[0]);
;             G8_BAR; G8_WAIT_L(0); G8_MMA(1, 0, At, B0); G8_BAR; G8_SCHED;
;             G8_STAGE(G8_SB(1, 1), b3 + hstep, voffB);
;             G8_WAIT_V(6); G8_BAR; G8_MMA(1, 1, At, B1); G8_BAR;
;         }
	s_waitcnt lgkmcnt(0)
	s_setprio 1
	s_waitcnt lgkmcnt(0)
	v_mfma_f32_16x16x32_bf16 v[118:121], v[216:219], v[168:171], v[118:121]
	v_mfma_f32_16x16x32_bf16 v[114:117], v[224:227], v[168:171], v[114:117]
	v_mfma_f32_16x16x32_bf16 v[102:105], v[216:219], v[176:179], v[102:105]
	v_mfma_f32_16x16x32_bf16 v[98:101], v[224:227], v[176:179], v[98:101]
	v_mfma_f32_16x16x32_bf16 v[86:89], v[216:219], v[184:187], v[86:89]
	v_mfma_f32_16x16x32_bf16 v[82:85], v[224:227], v[184:187], v[82:85]
	v_mfma_f32_16x16x32_bf16 v[70:73], v[216:219], v[192:195], v[70:73]
	v_mfma_f32_16x16x32_bf16 v[66:69], v[224:227], v[192:195], v[66:69]
	v_mfma_f32_16x16x32_bf16 v[118:121], v[220:223], v[172:175], v[118:121]
	v_mfma_f32_16x16x32_bf16 v[114:117], v[228:231], v[172:175], v[114:117]
	v_mfma_f32_16x16x32_bf16 v[102:105], v[220:223], v[180:183], v[102:105]
	v_mfma_f32_16x16x32_bf16 v[98:101], v[228:231], v[180:183], v[98:101]
	v_mfma_f32_16x16x32_bf16 v[86:89], v[220:223], v[188:191], v[86:89]
	v_mfma_f32_16x16x32_bf16 v[82:85], v[228:231], v[188:191], v[82:85]
	v_mfma_f32_16x16x32_bf16 v[70:73], v[220:223], v[196:199], v[70:73]
	v_mfma_f32_16x16x32_bf16 v[66:69], v[228:231], v[196:199], v[66:69]
	s_setprio 0
	s_mov_b32 m0, s48
	v_lshl_add_u64 v[144:145], v[232:233], 0, s[18:19]
	s_barrier
	ds_read_b128 v[168:171], v150 offset:49152
	ds_read_b128 v[172:175], v150 offset:50176
	ds_read_b128 v[176:179], v150 offset:51200
	ds_read_b128 v[180:183], v150 offset:52224
	ds_read_b128 v[184:187], v150 offset:53248
	ds_read_b128 v[188:191], v150 offset:54272
	ds_read_b128 v[192:195], v150 offset:55296
	ds_read_b128 v[196:199], v150 offset:56320
	global_load_lds_dwordx4 v[144:145], off
	v_lshl_add_u64 v[144:145], v[234:235], 0, s[18:19]
	s_mov_b32 m0, s49
	s_nop 0
	global_load_lds_dwordx4 v[144:145], off
	s_barrier
	s_waitcnt lgkmcnt(0)
	s_setprio 1
	s_waitcnt lgkmcnt(0)
	v_mfma_f32_16x16x32_bf16 v[62:65], v[152:155], v[168:171], v[62:65]
	v_mfma_f32_16x16x32_bf16 v[58:61], v[160:163], v[168:171], v[58:61]
	v_mfma_f32_16x16x32_bf16 v[46:49], v[152:155], v[176:179], v[46:49]
	v_mfma_f32_16x16x32_bf16 v[42:45], v[160:163], v[176:179], v[42:45]
	v_mfma_f32_16x16x32_bf16 v[30:33], v[152:155], v[184:187], v[30:33]
	v_mfma_f32_16x16x32_bf16 v[26:29], v[160:163], v[184:187], v[26:29]
	v_mfma_f32_16x16x32_bf16 v[14:17], v[152:155], v[192:195], v[14:17]
	v_mfma_f32_16x16x32_bf16 v[10:13], v[160:163], v[192:195], v[10:13]
	v_mfma_f32_16x16x32_bf16 v[62:65], v[156:159], v[172:175], v[62:65]
	v_mfma_f32_16x16x32_bf16 v[58:61], v[164:167], v[172:175], v[58:61]
	v_mfma_f32_16x16x32_bf16 v[46:49], v[156:159], v[180:183], v[46:49]
	v_mfma_f32_16x16x32_bf16 v[42:45], v[164:167], v[180:183], v[42:45]
	v_mfma_f32_16x16x32_bf16 v[30:33], v[156:159], v[188:191], v[30:33]
	v_mfma_f32_16x16x32_bf16 v[26:29], v[164:167], v[188:191], v[26:29]
	v_mfma_f32_16x16x32_bf16 v[14:17], v[156:159], v[196:199], v[14:17]
	v_mfma_f32_16x16x32_bf16 v[10:13], v[164:167], v[196:199], v[10:13]
	s_setprio 0
	s_barrier
	s_add_i32 s22, s22, s43
	v_lshl_add_u64 v[144:145], v[236:237], 0, s[18:19]
	s_mov_b32 m0, s22
	s_nop 0
	global_load_lds_dwordx4 v[144:145], off
	v_lshl_add_u64 v[144:145], v[238:239], 0, s[18:19]
	s_add_i32 m0, s22, 0x2000
	s_nop 0
	global_load_lds_dwordx4 v[144:145], off
	s_waitcnt vmcnt(6)
	s_barrier
	s_setprio 1
	v_mfma_f32_16x16x32_bf16 v[54:57], v[216:219], v[168:171], v[54:57]
	v_mfma_f32_16x16x32_bf16 v[50:53], v[224:227], v[168:171], v[50:53]
	v_mfma_f32_16x16x32_bf16 v[38:41], v[216:219], v[176:179], v[38:41]
	v_mfma_f32_16x16x32_bf16 v[34:37], v[224:227], v[176:179], v[34:37]
	v_mfma_f32_16x16x32_bf16 v[22:25], v[216:219], v[184:187], v[22:25]
	v_mfma_f32_16x16x32_bf16 v[18:21], v[224:227], v[184:187], v[18:21]
	v_mfma_f32_16x16x32_bf16 v[6:9], v[216:219], v[192:195], v[6:9]
	v_mfma_f32_16x16x32_bf16 v[2:5], v[224:227], v[192:195], v[2:5]
	v_mfma_f32_16x16x32_bf16 v[54:57], v[220:223], v[172:175], v[54:57]
	v_mfma_f32_16x16x32_bf16 v[50:53], v[228:231], v[172:175], v[50:53]
	v_mfma_f32_16x16x32_bf16 v[38:41], v[220:223], v[180:183], v[38:41]
	v_mfma_f32_16x16x32_bf16 v[34:37], v[228:231], v[180:183], v[34:37]
	v_mfma_f32_16x16x32_bf16 v[22:25], v[220:223], v[188:191], v[22:25]
	v_mfma_f32_16x16x32_bf16 v[18:21], v[228:231], v[188:191], v[18:21]
	v_mfma_f32_16x16x32_bf16 v[6:9], v[220:223], v[196:199], v[6:9]
	v_mfma_f32_16x16x32_bf16 v[2:5], v[228:231], v[196:199], v[2:5]
	s_setprio 0
	s_add_u32 s12, s12, 0x100
	s_addc_u32 s13, s13, 0
	s_add_u32 s58, s58, 0x100
	s_addc_u32 s59, s59, 0
	s_cmp_ge_u32 s60, s50
	s_mov_b32 s22, s60
	s_barrier
	s_cbranch_scc0 .LBB0_2252
; __device__ __forceinline__ unsigned cvt_pk_bf16(float lo, float hi) { unsigned r; asm volatile("v_cvt_pk_bf16_f32 %0, %1, %2" : "=v"(r) : "v"(lo), "v"(hi)); return r; }
;     __device__ __forceinline__ void init(f32x4 (&acc)[2][2][4][2], const Unit& u, int wc, int fq) const {
;         const int col0 = u.pn * BM + wc * 32 + 8 * fq;
; #pragma unroll
;         for (int b = 0; b < 2; ++b)
; #pragma unroll
;             for (int n = 0; n < 2; ++n) { const f32x4 bv = *(const f32x4*)(bias + col0 + b * HALF + 4 * n);
; #pragma unroll
;                 for (int a = 0; a < 2; ++a)
; #pragma unroll
;                     for (int m = 0; m < 4; ++m) acc[a][b][m][n] = bv; } }
;     __device__ __forceinline__ void operator()(const f32x4 (&acc)[2][2][4][2], const Unit& u, int wr, int wc, int fr, int fq) const {
;         const int row0 = u.pm * BM + wr * 64 + fr, col0 = u.pn * BM + wc * 32 + 8 * fq;
; #pragma unroll
;         for (int ai = 0; ai < 2; ++ai)
; #pragma unroll
;             for (int m = 0; m < 4; ++m) { bf16_t* rowp = O + (size_t)(row0 + ai * HALF + m * 16) * ldc + col0;
; #pragma unroll
;                 for (int bj = 0; bj < 2; ++bj) { const f32x4 v0 = acc[ai][bj][m][0], v1 = acc[ai][bj][m][1];
;                     u32x4 w; w[0] = cvt_pk_bf16(v0[0], v0[1]); w[1] = cvt_pk_bf16(v0[2], v0[3]); w[2] = cvt_pk_bf16(v1[0], v1[1]); w[3] = cvt_pk_bf16(v1[2], v1[3]);
;                     *(u32x4*)(rowp + bj * HALF) = w; } }
;     }
	s_nop 0
	s_nop 0
	s_nop 0
	s_nop 0
	s_nop 0
	s_nop 0
	s_nop 0
	s_nop 0
	s_nop 0
	v_lshl_add_u32 v152, s56, 8, v147
	v_lshl_or_b32 v144, s57, 8, v149
	v_ashrrev_i32_e32 v153, 31, v152
	v_ashrrev_i32_e32 v145, 31, v144
	v_lshlrev_b64 v[154:155], 11, v[152:153]
	v_lshl_add_u64 v[154:155], s[4:5], 0, v[154:155]
	v_lshlrev_b64 v[156:157], 1, v[144:145]
	v_lshl_add_u64 v[144:145], v[154:155], 0, v[156:157]
	v_cvt_pk_bf16_f32 v126, v126, v127
	v_cvt_pk_bf16_f32 v127, v128, v129
	v_cvt_pk_bf16_f32 v128, v122, v123
	v_cvt_pk_bf16_f32 v129, v124, v125
	global_store_dwordx4 v[144:145], v[126:129], off
	v_cvt_pk_bf16_f32 v118, v118, v119
	v_cvt_pk_bf16_f32 v119, v120, v121
	v_cvt_pk_bf16_f32 v120, v114, v115
	v_or_b32_e32 v114, 16, v152
	v_ashrrev_i32_e32 v115, 31, v114
	v_lshlrev_b64 v[114:115], 11, v[114:115]
	v_lshl_add_u64 v[114:115], s[4:5], 0, v[114:115]
	v_lshl_add_u64 v[114:115], v[114:115], 0, v[156:157]
	v_cvt_pk_bf16_f32 v121, v116, v117
	global_store_dwordx4 v[144:145], v[118:121], off offset:256
	v_cvt_pk_bf16_f32 v110, v110, v111
	v_cvt_pk_bf16_f32 v111, v112, v113
	v_cvt_pk_bf16_f32 v112, v106, v107
	v_cvt_pk_bf16_f32 v113, v108, v109
	global_store_dwordx4 v[114:115], v[110:113], off
	v_cvt_pk_bf16_f32 v102, v102, v103
	v_cvt_pk_bf16_f32 v103, v104, v105
	v_cvt_pk_bf16_f32 v104, v98, v99
	v_or_b32_e32 v98, 32, v152
	v_ashrrev_i32_e32 v99, 31, v98
	v_lshlrev_b64 v[98:99], 11, v[98:99]
	v_lshl_add_u64 v[98:99], s[4:5], 0, v[98:99]
	v_lshl_add_u64 v[98:99], v[98:99], 0, v[156:157]
	v_cvt_pk_bf16_f32 v105, v100, v101
	global_store_dwordx4 v[114:115], v[102:105], off offset:256
	v_cvt_pk_bf16_f32 v94, v94, v95
	v_cvt_pk_bf16_f32 v95, v96, v97
	v_cvt_pk_bf16_f32 v96, v90, v91
	v_cvt_pk_bf16_f32 v97, v92, v93
	global_store_dwordx4 v[98:99], v[94:97], off
	v_cvt_pk_bf16_f32 v86, v86, v87
	v_cvt_pk_bf16_f32 v87, v88, v89
	v_cvt_pk_bf16_f32 v88, v82, v83
	v_or_b32_e32 v82, 48, v152
	v_ashrrev_i32_e32 v83, 31, v82
	v_lshlrev_b64 v[82:83], 11, v[82:83]
	v_lshl_add_u64 v[82:83], s[4:5], 0, v[82:83]
	v_lshl_add_u64 v[82:83], v[82:83], 0, v[156:157]
	s_mov_b64 s[0:1], 0x40000
	v_cvt_pk_bf16_f32 v89, v84, v85
	global_store_dwordx4 v[98:99], v[86:89], off offset:256
	v_cvt_pk_bf16_f32 v78, v78, v79
	v_cvt_pk_bf16_f32 v79, v80, v81
	v_cvt_pk_bf16_f32 v80, v74, v75
	v_cvt_pk_bf16_f32 v81, v76, v77
	global_store_dwordx4 v[82:83], v[78:81], off
	v_cvt_pk_bf16_f32 v70, v70, v71
	v_cvt_pk_bf16_f32 v71, v72, v73
	v_cvt_pk_bf16_f32 v72, v66, v67
	v_cvt_pk_bf16_f32 v73, v68, v69
	global_store_dwordx4 v[82:83], v[70:73], off offset:256
	v_lshl_add_u64 v[66:67], v[144:145], 0, s[0:1]
	v_cvt_pk_bf16_f32 v62, v62, v63
	v_cvt_pk_bf16_f32 v63, v64, v65
	v_cvt_pk_bf16_f32 v64, v58, v59
	v_add_co_u32_e64 v58, s[0:1], s82, v144
	v_cvt_pk_bf16_f32 v65, v60, v61
	s_and_b64 vcc, exec, vcc
	s_nop 0
	v_addc_co_u32_e64 v59, s[0:1], 0, v145, s[0:1]
	s_mov_b64 s[0:1], 0x48000
	global_store_dwordx4 v[58:59], v[62:65], off
	v_cvt_pk_bf16_f32 v54, v54, v55
	v_cvt_pk_bf16_f32 v55, v56, v57
	v_cvt_pk_bf16_f32 v56, v50, v51
	v_lshl_add_u64 v[50:51], v[144:145], 0, s[0:1]
	s_mov_b32 s0, 0x48000
	v_cvt_pk_bf16_f32 v57, v52, v53
	global_store_dwordx4 v[66:67], v[54:57], off offset:256
	v_cvt_pk_bf16_f32 v46, v46, v47
	v_cvt_pk_bf16_f32 v47, v48, v49
	v_cvt_pk_bf16_f32 v48, v42, v43
	v_add_co_u32_e64 v42, s[0:1], s0, v144
	v_cvt_pk_bf16_f32 v49, v44, v45
	s_nop 1
	v_addc_co_u32_e64 v43, s[0:1], 0, v145, s[0:1]
	s_mov_b64 s[0:1], 0x50000
	global_store_dwordx4 v[42:43], v[46:49], off
	v_cvt_pk_bf16_f32 v38, v38, v39
	v_cvt_pk_bf16_f32 v39, v40, v41
	v_cvt_pk_bf16_f32 v40, v34, v35
	v_lshl_add_u64 v[34:35], v[144:145], 0, s[0:1]
	s_mov_b32 s0, 0x50000
	v_cvt_pk_bf16_f32 v41, v36, v37
	global_store_dwordx4 v[50:51], v[38:41], off offset:256
	v_cvt_pk_bf16_f32 v30, v30, v31
	v_cvt_pk_bf16_f32 v31, v32, v33
	v_cvt_pk_bf16_f32 v32, v26, v27
	v_add_co_u32_e64 v26, s[0:1], s0, v144
	v_cvt_pk_bf16_f32 v33, v28, v29
	s_nop 1
	v_addc_co_u32_e64 v27, s[0:1], 0, v145, s[0:1]
	s_mov_b64 s[0:1], 0x58000
	global_store_dwordx4 v[26:27], v[30:33], off
	v_cvt_pk_bf16_f32 v22, v22, v23
	v_cvt_pk_bf16_f32 v23, v24, v25
	v_cvt_pk_bf16_f32 v24, v18, v19
	v_lshl_add_u64 v[18:19], v[144:145], 0, s[0:1]
	s_mov_b32 s0, 0x58000
	v_cvt_pk_bf16_f32 v25, v20, v21
	global_store_dwordx4 v[34:35], v[22:25], off offset:256
	v_cvt_pk_bf16_f32 v14, v14, v15
	v_cvt_pk_bf16_f32 v15, v16, v17
	v_cvt_pk_bf16_f32 v16, v10, v11
	v_add_co_u32_e64 v10, s[0:1], s0, v144
	v_cvt_pk_bf16_f32 v17, v12, v13
	s_nop 1
	v_addc_co_u32_e64 v11, s[0:1], 0, v145, s[0:1]
	global_store_dwordx4 v[10:11], v[14:17], off
	v_cvt_pk_bf16_f32 v6, v6, v7
	v_cvt_pk_bf16_f32 v7, v8, v9
	v_cvt_pk_bf16_f32 v8, v2, v3
	v_cvt_pk_bf16_f32 v9, v4, v5
	s_mov_b64 s[0:1], -1
	global_store_dwordx4 v[18:19], v[6:9], off offset:256
	s_cbranch_vccz .LBB0_2244
	v_lshl_or_b32 v2, s54, 8, v149
	v_ashrrev_i32_e32 v3, 31, v2
	v_lshl_add_u64 v[6:7], v[2:3], 2, s[2:3]
	global_load_dwordx4 v[10:13], v[6:7], off offset:16
	global_load_dwordx4 v[14:17], v[6:7], off
	global_load_dwordx4 v[2:5], v[6:7], off offset:528
	s_nop 0
	global_load_dwordx4 v[6:9], v[6:7], off offset:512
	s_mov_b64 s[0:1], 0
	s_branch .LBB0_2244
